# norm2+router rows: the sum-of-squares and abs-max wave reductions use DPP row ops + permlane16/32 swaps (same pairing order, bit-identical) instead of six dependent ds_bpermute round trips
# speedup vs baseline: 1.0007x; 1.0007x over previous
.LBB0_1693:
	s_add_i32 s14, s29, s47
	s_add_i32 s16, s14, -8
	s_min_i32 s15, s16, 0x4000
	s_ashr_i32 s15, s15, 13
	s_mul_i32 s18, s15, 0x3000
	s_ashr_i32 s17, s16, 31
	s_ashr_i32 s19, s18, 31
	s_lshl_b64 s[22:23], s[16:17], 11
	s_lshl_b64 s[18:19], s[18:19], 2
	s_add_u32 s15, s33, s18
	s_addc_u32 s26, s34, s19
	s_add_u32 s18, s15, 0x4000
	s_addc_u32 s19, s26, 0
	s_waitcnt lgkmcnt(0)
	s_add_u32 s100, s15, 0x6000
	s_addc_u32 s101, s26, 0
	s_add_u32 s98, s15, 0x8000
	s_addc_u32 s99, s26, 0
	global_load_dwordx4 v[132:135], v240, s[18:19]
	global_load_dwordx4 v[136:139], v241, s[18:19]
	global_load_dwordx4 v[140:143], v242, s[18:19]
	global_load_dwordx4 v[144:147], v243, s[18:19]
	global_load_dwordx4 v[148:151], v244, s[18:19]
	global_load_dwordx4 v[152:155], v245, s[18:19]
	global_load_dwordx4 v[156:159], v246, s[18:19]
	global_load_dwordx4 v[160:163], v247, s[18:19]
	global_load_dwordx4 v[164:167], v[82:83], off
	global_load_dwordx4 v[168:171], v240, s[100:101]
	global_load_dwordx4 v[172:175], v240, s[98:99]
	global_load_dwordx4 v[176:179], v[82:83], off offset:1024
	global_load_dwordx4 v[196:199], v241, s[100:101]
	global_load_dwordx4 v[200:203], v241, s[98:99]
	global_load_dwordx4 v[204:207], v[82:83], off offset:2048
	global_load_dwordx4 v[208:211], v242, s[100:101]
	global_load_dwordx4 v[212:215], v242, s[98:99]
	global_load_dwordx4 v[216:219], v[82:83], off offset:3072
	global_load_dwordx4 v[220:223], v243, s[100:101]
	global_load_dwordx4 v[224:227], v243, s[98:99]
	global_load_dwordx4 v[228:231], v[84:85], off
	global_load_dwordx4 v[232:235], v244, s[100:101]
	global_load_dwordx4 v[236:239], v244, s[98:99]
	global_load_dwordx4 v[252:255], v[86:87], off
	s_waitcnt vmcnt(32)
	v_lshlrev_b32_e32 v2, 16, v18
	v_and_b32_e32 v3, 0xffff0000, v18
	s_waitcnt vmcnt(28)
	v_lshlrev_b32_e32 v8, 16, v26
	v_and_b32_e32 v9, 0xffff0000, v26
	s_lshl_b64 s[24:25], s[16:17], 12
	v_lshl_add_u64 v[118:119], v[92:93], 0, s[24:25]
	s_waitcnt vmcnt(27)
	v_lshlrev_b32_e32 v12, 16, v28
	v_and_b32_e32 v13, 0xffff0000, v28
	s_waitcnt vmcnt(25)
	v_lshlrev_b32_e32 v104, 16, v32
	v_and_b32_e32 v105, 0xffff0000, v32
	s_waitcnt vmcnt(20)
	v_lshlrev_b32_e32 v108, 16, v42
	v_and_b32_e32 v109, 0xffff0000, v42
	v_lshlrev_b32_e32 v128, 16, v40
	v_and_b32_e32 v129, 0xffff0000, v40
	s_waitcnt vmcnt(17)
	v_lshlrev_b32_e32 v130, 16, v48
	v_and_b32_e32 v131, 0xffff0000, v48
	s_add_u32 s24, s15, 0x6000
	s_addc_u32 s25, s26, 0
	s_waitcnt vmcnt(23)
	v_pk_fma_f32 v[4:5], v[132:133], v[8:9], v[2:3]
	v_lshlrev_b32_e32 v2, 16, v19
	v_and_b32_e32 v3, 0xffff0000, v19
	v_lshlrev_b32_e32 v8, 16, v27
	v_and_b32_e32 v9, 0xffff0000, v27
	v_pk_fma_f32 v[10:11], v[134:135], v[8:9], v[2:3]
	v_cvt_pk_bf16_f32 v2, v4, v5
	v_cvt_pk_bf16_f32 v3, v10, v11
	global_store_dwordx2 v[118:119], v[2:3], off nt
	v_lshlrev_b32_e32 v2, 16, v20
	v_and_b32_e32 v3, 0xffff0000, v20
	v_mov_b32_e32 v98, v11
	s_waitcnt vmcnt(23)
	v_pk_fma_f32 v[2:3], v[136:137], v[12:13], v[2:3]
	v_lshlrev_b32_e32 v6, 16, v21
	v_and_b32_e32 v7, 0xffff0000, v21
	v_lshlrev_b32_e32 v12, 16, v29
	v_and_b32_e32 v13, 0xffff0000, v29
	v_pk_fma_f32 v[6:7], v[138:139], v[12:13], v[6:7]
	v_cvt_pk_bf16_f32 v8, v2, v3
	v_cvt_pk_bf16_f32 v9, v6, v7
	v_mov_b32_e32 v12, v5
	v_mov_b32_e32 v13, v3
	global_store_dwordx2 v[118:119], v[8:9], off offset:512 nt
	v_mov_b32_e32 v8, v4
	v_mov_b32_e32 v9, v2
	v_pk_mul_f32 v[12:13], v[12:13], v[12:13]
	v_mov_b32_e32 v99, v7
	v_pk_fma_f32 v[8:9], v[8:9], v[8:9], v[12:13]
	v_mov_b32_e32 v12, v10
	v_mov_b32_e32 v13, v6
	v_pk_mul_f32 v[98:99], v[98:99], v[98:99]
	s_nop 0
	v_pk_fma_f32 v[12:13], v[12:13], v[12:13], v[98:99]
	v_pk_add_f32 v[8:9], v[8:9], v[12:13]
	v_lshlrev_b32_e32 v12, 16, v30
	v_pk_add_f32 v[102:103], v[8:9], v[8:9] op_sel:[0,1] op_sel_hi:[1,0]
	v_lshlrev_b32_e32 v8, 16, v22
	v_and_b32_e32 v9, 0xffff0000, v22
	v_and_b32_e32 v13, 0xffff0000, v30
	s_waitcnt vmcnt(23)
	v_pk_fma_f32 v[12:13], v[140:141], v[12:13], v[8:9]
	v_lshlrev_b32_e32 v8, 16, v23
	v_and_b32_e32 v9, 0xffff0000, v23
	v_lshlrev_b32_e32 v98, 16, v31
	v_and_b32_e32 v99, 0xffff0000, v31
	v_pk_fma_f32 v[110:111], v[142:143], v[98:99], v[8:9]
	v_cvt_pk_bf16_f32 v8, v12, v13
	v_cvt_pk_bf16_f32 v9, v110, v111
	v_mov_b32_e32 v98, v13
	v_mov_b32_e32 v99, v111
	global_store_dwordx2 v[118:119], v[8:9], off offset:1024 nt
	v_mov_b32_e32 v8, v12
	v_mov_b32_e32 v9, v110
	v_pk_mul_f32 v[98:99], v[98:99], v[98:99]
	s_nop 0
	v_pk_fma_f32 v[8:9], v[8:9], v[8:9], v[98:99]
	v_pk_add_f32 v[106:107], v[8:9], v[8:9] op_sel:[0,1] op_sel_hi:[1,0]
	v_lshlrev_b32_e32 v8, 16, v24
	v_and_b32_e32 v9, 0xffff0000, v24
	s_waitcnt vmcnt(23)
	v_pk_fma_f32 v[104:105], v[144:145], v[104:105], v[8:9]
	v_lshlrev_b32_e32 v8, 16, v25
	v_and_b32_e32 v9, 0xffff0000, v25
	v_lshlrev_b32_e32 v98, 16, v33
	v_and_b32_e32 v99, 0xffff0000, v33
	v_pk_fma_f32 v[114:115], v[146:147], v[98:99], v[8:9]
	v_cvt_pk_bf16_f32 v8, v104, v105
	v_cvt_pk_bf16_f32 v9, v114, v115
	global_store_dwordx2 v[118:119], v[8:9], off offset:1536 nt
	v_mul_f32_e32 v8, v105, v105
	v_pk_fma_f32 v[112:113], v[104:105], v[104:105], v[8:9] op_sel_hi:[1,1,0]
	v_mul_f32_e32 v8, v115, v115
	v_pk_fma_f32 v[116:117], v[114:115], v[114:115], v[8:9] op_sel_hi:[1,1,0]
	v_lshlrev_b32_e32 v8, 16, v34
	v_and_b32_e32 v9, 0xffff0000, v34
	s_waitcnt vmcnt(23)
	v_pk_fma_f32 v[8:9], v[148:149], v[108:109], v[8:9]
	v_lshlrev_b32_e32 v98, 16, v35
	v_and_b32_e32 v99, 0xffff0000, v35
	v_lshlrev_b32_e32 v108, 16, v43
	v_and_b32_e32 v109, 0xffff0000, v43
	v_pk_fma_f32 v[108:109], v[150:151], v[108:109], v[98:99]
	v_cvt_pk_bf16_f32 v98, v8, v9
	v_cvt_pk_bf16_f32 v99, v108, v109
	global_store_dwordx2 v[118:119], v[98:99], off offset:2048 nt
	v_pk_mul_f32 v[98:99], v[8:9], v[8:9]
	v_pk_mul_f32 v[100:101], v[108:109], v[108:109]
	v_mov_b32_e32 v103, v98
	v_mov_b32_e32 v107, v99
	v_mov_b32_e32 v113, v100
	v_mov_b32_e32 v117, v101
	v_pk_add_f32 v[98:99], v[102:103], v[106:107]
	v_pk_add_f32 v[100:101], v[112:113], v[116:117]
	v_lshlrev_b32_e32 v102, 16, v36
	v_pk_add_f32 v[98:99], v[98:99], v[100:101]
	v_and_b32_e32 v103, 0xffff0000, v36
	v_pk_add_f32 v[120:121], v[98:99], v[98:99] op_sel:[0,1] op_sel_hi:[1,0]
	v_lshlrev_b32_e32 v106, 16, v44
	v_and_b32_e32 v107, 0xffff0000, v44
	v_lshlrev_b32_e32 v112, 16, v46
	v_and_b32_e32 v113, 0xffff0000, v46
	s_waitcnt vmcnt(23)
	v_pk_fma_f32 v[106:107], v[152:153], v[106:107], v[102:103]
	v_lshlrev_b32_e32 v98, 16, v37
	v_and_b32_e32 v99, 0xffff0000, v37
	v_lshlrev_b32_e32 v102, 16, v45
	v_and_b32_e32 v103, 0xffff0000, v45
	v_pk_fma_f32 v[116:117], v[154:155], v[102:103], v[98:99]
	v_cvt_pk_bf16_f32 v98, v106, v107
	v_cvt_pk_bf16_f32 v99, v116, v117
	v_mov_b32_e32 v100, v107
	v_mov_b32_e32 v101, v117
	global_store_dwordx2 v[118:119], v[98:99], off offset:2560 nt
	v_mov_b32_e32 v98, v106
	v_mov_b32_e32 v99, v116
	v_pk_mul_f32 v[100:101], v[100:101], v[100:101]
	v_lshlrev_b32_e32 v102, 16, v38
	v_pk_fma_f32 v[98:99], v[98:99], v[98:99], v[100:101]
	v_and_b32_e32 v103, 0xffff0000, v38
	v_pk_add_f32 v[122:123], v[98:99], v[98:99] op_sel:[0,1] op_sel_hi:[1,0]
	s_waitcnt vmcnt(23)
	v_pk_fma_f32 v[102:103], v[156:157], v[112:113], v[102:103]
	v_lshlrev_b32_e32 v98, 16, v39
	v_and_b32_e32 v99, 0xffff0000, v39
	v_lshlrev_b32_e32 v112, 16, v47
	v_and_b32_e32 v113, 0xffff0000, v47
	v_pk_fma_f32 v[112:113], v[158:159], v[112:113], v[98:99]
	v_cvt_pk_bf16_f32 v98, v102, v103
	v_cvt_pk_bf16_f32 v99, v112, v113
	global_store_dwordx2 v[118:119], v[98:99], off offset:3072 nt
	v_mul_f32_e32 v16, v103, v103
	v_pk_fma_f32 v[124:125], v[102:103], v[102:103], v[16:17] op_sel_hi:[1,1,0]
	v_mul_f32_e32 v16, v113, v113
	v_pk_fma_f32 v[126:127], v[112:113], v[112:113], v[16:17] op_sel_hi:[1,1,0]
	s_add_u32 s18, s15, 0x8000
	s_addc_u32 s19, s26, 0
	s_waitcnt vmcnt(23)
	v_pk_fma_f32 v[98:99], v[160:161], v[130:131], v[128:129]
	v_lshlrev_b32_e32 v128, 16, v41
	v_and_b32_e32 v129, 0xffff0000, v41
	v_lshlrev_b32_e32 v130, 16, v49
	v_and_b32_e32 v131, 0xffff0000, v49
	v_pk_fma_f32 v[100:101], v[162:163], v[130:131], v[128:129]
	global_load_dwordx4 v[160:163], v245, s[100:101]
	v_cvt_pk_bf16_f32 v128, v98, v99
	v_cvt_pk_bf16_f32 v129, v100, v101
	global_store_dwordx2 v[118:119], v[128:129], off offset:3584 nt
	v_pk_mul_f32 v[118:119], v[98:99], v[98:99]
	v_pk_mul_f32 v[128:129], v[100:101], v[100:101]
	v_mov_b32_e32 v121, v118
	v_mov_b32_e32 v123, v119
	v_mov_b32_e32 v125, v128
	v_mov_b32_e32 v127, v129
	v_pk_add_f32 v[118:119], v[120:121], v[122:123]
	v_pk_add_f32 v[120:121], v[124:125], v[126:127]
	s_nop 0
	v_pk_add_f32 v[118:119], v[118:119], v[120:121]
	s_nop 0
	v_add_f32_e32 v16, v118, v119
	s_waitcnt lgkmcnt(0)
	s_nop 1
	v_add_f32_dpp v16, v16, v16 quad_perm:[1,0,3,2] row_mask:0xf bank_mask:0xf
	s_nop 1
	v_add_f32_dpp v16, v16, v16 quad_perm:[2,3,0,1] row_mask:0xf bank_mask:0xf
	s_nop 1
	v_add_f32_dpp v16, v16, v16 row_half_mirror row_mask:0xf bank_mask:0xf
	s_nop 1
	v_add_f32_dpp v16, v16, v16 row_mirror row_mask:0xf bank_mask:0xf
	v_mov_b32_e32 v118, v16
	s_nop 1
	v_permlane16_swap_b32 v118, v16
	v_add_f32_e32 v16, v118, v16
	v_mov_b32_e32 v118, v16
	s_nop 1
	v_permlane32_swap_b32 v118, v16
	v_add_f32_e32 v16, v118, v16
	v_fmamk_f32 v16, v16, 0x3a000000, v248
	v_cmp_gt_f32_e32 vcc, s51, v16
	v_mul_f32_e32 v118, 0x4b800000, v16
	s_nop 0
	v_cndmask_b32_e32 v16, v16, v118, vcc
	v_rsq_f32_e32 v16, v16
	s_nop 0
	v_mul_f32_e32 v118, 0x45800000, v16
	v_cndmask_b32_e32 v16, v16, v118, vcc
	v_pk_mul_f32 v[10:11], v[10:11], v[16:17] op_sel_hi:[1,0]
	v_pk_mul_f32 v[4:5], v[4:5], v[16:17] op_sel_hi:[1,0]
	v_pk_mul_f32 v[2:3], v[2:3], v[16:17] op_sel_hi:[1,0]
	v_pk_mul_f32 v[104:105], v[104:105], v[16:17] op_sel_hi:[1,0]
	v_pk_mul_f32 v[8:9], v[8:9], v[16:17] op_sel_hi:[1,0]
	v_pk_mul_f32 v[106:107], v[106:107], v[16:17] op_sel_hi:[1,0]
	v_pk_mul_f32 v[102:103], v[102:103], v[16:17] op_sel_hi:[1,0]
	v_pk_mul_f32 v[100:101], v[100:101], v[16:17] op_sel_hi:[1,0]
	v_pk_mul_f32 v[98:99], v[98:99], v[16:17] op_sel_hi:[1,0]
	s_waitcnt vmcnt(24)
	v_pk_mul_f32 v[4:5], v[164:165], v[4:5]
	v_pk_mul_f32 v[10:11], v[166:167], v[10:11]
	global_load_dwordx4 v[164:167], v245, s[98:99]
	s_waitcnt vmcnt(23)
	v_pk_add_f32 v[118:119], v[174:175], 1.0 op_sel_hi:[1,0]
	v_pk_add_f32 v[120:121], v[172:173], 1.0 op_sel_hi:[1,0]
	global_load_dwordx4 v[172:175], v[88:89], off
	v_pk_fma_f32 v[128:129], v[118:119], v[10:11], v[170:171]
	v_pk_fma_f32 v[130:131], v[120:121], v[4:5], v[168:169]
	global_load_dwordx4 v[168:171], v246, s[100:101]
	v_max_f32_e64 v4, |v128|, |v129|
	v_max3_f32 v136, |v130|, |v131|, v4
	v_pk_mul_f32 v[4:5], v[6:7], v[16:17] op_sel_hi:[1,0]
	s_waitcnt vmcnt(24)
	v_pk_mul_f32 v[2:3], v[176:177], v[2:3]
	v_pk_mul_f32 v[4:5], v[178:179], v[4:5]
	global_load_dwordx4 v[176:179], v246, s[98:99]
	s_waitcnt vmcnt(23)
	v_pk_add_f32 v[6:7], v[202:203], 1.0 op_sel_hi:[1,0]
	v_pk_add_f32 v[10:11], v[200:201], 1.0 op_sel_hi:[1,0]
	global_load_dwordx4 v[200:203], v[90:91], off
	v_pk_fma_f32 v[126:127], v[6:7], v[4:5], v[198:199]
	v_pk_fma_f32 v[132:133], v[10:11], v[2:3], v[196:197]
	global_load_dwordx4 v[196:199], v247, s[100:101]
	v_max_f32_e64 v2, |v126|, |v127|
	v_max3_f32 v2, |v132|, |v133|, v2
	v_max3_f32 v142, v136, 0, v2
	v_pk_mul_f32 v[6:7], v[110:111], v[16:17] op_sel_hi:[1,0]
	v_pk_mul_f32 v[10:11], v[12:13], v[16:17] op_sel_hi:[1,0]
	s_waitcnt vmcnt(24)
	v_pk_mul_f32 v[4:5], v[206:207], v[6:7]
	v_pk_mul_f32 v[2:3], v[204:205], v[10:11]
	global_load_dwordx4 v[204:207], v247, s[98:99]
	s_waitcnt vmcnt(23)
	v_pk_add_f32 v[6:7], v[214:215], 1.0 op_sel_hi:[1,0]
	v_pk_add_f32 v[10:11], v[212:213], 1.0 op_sel_hi:[1,0]
	v_pk_fma_f32 v[138:139], v[6:7], v[4:5], v[210:211]
	v_pk_fma_f32 v[140:141], v[10:11], v[2:3], v[208:209]
	v_max_f32_e64 v2, |v138|, |v139|
	v_max3_f32 v110, |v140|, |v141|, v2
	v_pk_mul_f32 v[6:7], v[114:115], v[16:17] op_sel_hi:[1,0]
	s_waitcnt vmcnt(22)
	v_pk_mul_f32 v[2:3], v[216:217], v[104:105]
	v_pk_mul_f32 v[4:5], v[218:219], v[6:7]
	s_waitcnt vmcnt(20)
	v_pk_add_f32 v[6:7], v[226:227], 1.0 op_sel_hi:[1,0]
	v_pk_add_f32 v[104:105], v[224:225], 1.0 op_sel_hi:[1,0]
	v_pk_fma_f32 v[134:135], v[6:7], v[4:5], v[222:223]
	v_pk_fma_f32 v[136:137], v[104:105], v[2:3], v[220:221]
	v_max_f32_e64 v2, |v134|, |v135|
	v_max3_f32 v2, |v136|, |v137|, v2
	v_max3_f32 v110, v142, v110, v2
	v_pk_mul_f32 v[6:7], v[108:109], v[16:17] op_sel_hi:[1,0]
	v_pk_mul_f32 v[104:105], v[116:117], v[16:17] op_sel_hi:[1,0]
	s_waitcnt vmcnt(19)
	v_pk_mul_f32 v[4:5], v[230:231], v[6:7]
	v_pk_mul_f32 v[2:3], v[228:229], v[8:9]
	s_waitcnt vmcnt(17)
	v_pk_add_f32 v[6:7], v[238:239], 1.0 op_sel_hi:[1,0]
	v_pk_add_f32 v[8:9], v[236:237], 1.0 op_sel_hi:[1,0]
	v_pk_fma_f32 v[144:145], v[4:5], v[6:7], v[234:235]
	v_pk_fma_f32 v[148:149], v[2:3], v[8:9], v[232:233]
	v_max_f32_e64 v2, |v144|, |v145|
	v_max3_f32 v108, |v148|, |v149|, v2
	s_waitcnt vmcnt(16)
	v_pk_mul_f32 v[4:5], v[104:105], v[254:255]
	v_pk_mul_f32 v[2:3], v[106:107], v[252:253]
	s_waitcnt vmcnt(6)
	v_pk_add_f32 v[12:13], v[166:167], 1.0 op_sel_hi:[1,0]
	v_pk_add_f32 v[10:11], v[164:165], 1.0 op_sel_hi:[1,0]
	v_pk_fma_f32 v[142:143], v[4:5], v[12:13], v[162:163]
	v_pk_fma_f32 v[146:147], v[2:3], v[10:11], v[160:161]
	v_max_f32_e64 v2, |v142|, |v143|
	v_max3_f32 v2, |v146|, |v147|, v2
	v_max3_f32 v104, v110, v108, v2
	v_pk_mul_f32 v[106:107], v[112:113], v[16:17] op_sel_hi:[1,0]
	s_waitcnt vmcnt(5)
	v_pk_mul_f32 v[2:3], v[102:103], v[172:173]
	v_pk_mul_f32 v[4:5], v[106:107], v[174:175]
	s_waitcnt vmcnt(3)
	v_pk_add_f32 v[12:13], v[178:179], 1.0 op_sel_hi:[1,0]
	v_pk_add_f32 v[10:11], v[176:177], 1.0 op_sel_hi:[1,0]
	v_pk_fma_f32 v[150:151], v[4:5], v[12:13], v[170:171]
	v_pk_fma_f32 v[152:153], v[2:3], v[10:11], v[168:169]
	v_max_f32_e64 v2, |v150|, |v151|
	v_max3_f32 v102, |v152|, |v153|, v2
	s_waitcnt vmcnt(2)
	v_pk_mul_f32 v[8:9], v[100:101], v[202:203]
	v_pk_mul_f32 v[6:7], v[98:99], v[200:201]
	s_waitcnt vmcnt(0)
	v_pk_add_f32 v[12:13], v[206:207], 1.0 op_sel_hi:[1,0]
	v_pk_add_f32 v[10:11], v[204:205], 1.0 op_sel_hi:[1,0]
	v_pk_fma_f32 v[154:155], v[8:9], v[12:13], v[198:199]
	v_pk_fma_f32 v[156:157], v[6:7], v[10:11], v[196:197]
	v_max_f32_e64 v2, |v154|, |v155|
	v_max3_f32 v2, |v156|, |v157|, v2
	v_max3_f32 v2, v104, v102, v2
	s_waitcnt lgkmcnt(0)
	s_nop 1
	v_max_f32_dpp v2, v2, v2 quad_perm:[1,0,3,2] row_mask:0xf bank_mask:0xf
	s_nop 1
	v_max_f32_dpp v2, v2, v2 quad_perm:[2,3,0,1] row_mask:0xf bank_mask:0xf
	s_nop 1
	v_max_f32_dpp v2, v2, v2 row_half_mirror row_mask:0xf bank_mask:0xf
	s_nop 1
	v_max_f32_dpp v2, v2, v2 row_mirror row_mask:0xf bank_mask:0xf
	v_mov_b32_e32 v3, v2
	s_nop 1
	v_permlane16_swap_b32 v3, v2
	v_max_f32_e32 v2, v3, v2
	ds_bpermute_b32 v3, v183, v2
	s_and_saveexec_b64 s[18:19], s[4:5]
	s_cbranch_execz .LBB0_1695
	s_waitcnt lgkmcnt(0)
	v_max_f32_e32 v3, v3, v3
	v_max_f32_e32 v2, v2, v2
	s_lshl_b64 s[16:17], s[16:17], 2
	v_max_f32_e32 v2, v2, v3
	s_add_u32 s16, s35, s16
	v_mul_f32_e32 v2, 0x3c010204, v2
	s_addc_u32 s17, s38, s17
	global_store_dword v17, v2, s[16:17]
.LBB0_1695:
	s_or_b64 exec, exec, s[18:19]
	v_mov_b32_e32 v4, 0
	v_cvt_pk_fp8_f32 v4, v130, v131
	s_waitcnt lgkmcnt(0)
	v_lshl_add_u64 v[2:3], v[94:95], 0, s[22:23]
	s_add_i32 s16, s50, s47
	s_add_i32 s18, s16, -8
	v_cvt_pk_fp8_f32 v4, v128, v129 op_sel:[0,0,1]
	s_min_i32 s15, s18, 0x4000
	s_ashr_i32 s15, s15, 13
	s_mul_i32 s22, s15, 0x3000
	global_store_dword v[2:3], v4, off
	v_mov_b32_e32 v4, 0
	v_cvt_pk_fp8_f32 v4, v132, v133
	s_ashr_i32 s23, s22, 31
	s_ashr_i32 s19, s18, 31
	s_lshl_b64 s[22:23], s[22:23], 2
	v_cvt_pk_fp8_f32 v4, v126, v127 op_sel:[0,0,1]
	s_add_u32 s15, s33, s22
	s_addc_u32 s17, s34, s23
	s_add_u32 s22, s15, 0x4000
	global_store_dword v[2:3], v4, off offset:256
	v_mov_b32_e32 v4, 0
	v_cvt_pk_fp8_f32 v4, v140, v141
	s_addc_u32 s23, s17, 0
	v_lshlrev_b32_e32 v8, 16, v58
	v_and_b32_e32 v9, 0xffff0000, v58
	v_cvt_pk_fp8_f32 v4, v138, v139 op_sel:[0,0,1]
	s_lshl_b64 s[24:25], s[18:19], 12
	v_lshl_add_u64 v[98:99], v[92:93], 0, s[24:25]
	v_lshlrev_b32_e32 v12, 16, v60
	global_store_dword v[2:3], v4, off offset:512
	v_mov_b32_e32 v4, 0
	v_cvt_pk_fp8_f32 v4, v136, v137
	v_and_b32_e32 v13, 0xffff0000, v60
	v_lshlrev_b32_e32 v110, 16, v64
	v_and_b32_e32 v111, 0xffff0000, v64
	v_cvt_pk_fp8_f32 v4, v134, v135 op_sel:[0,0,1]
	v_lshlrev_b32_e32 v114, 16, v74
	v_and_b32_e32 v115, 0xffff0000, v74
	v_lshlrev_b32_e32 v122, 16, v78
	global_store_dword v[2:3], v4, off offset:768
	v_mov_b32_e32 v4, 0
	v_cvt_pk_fp8_f32 v4, v148, v149
	v_and_b32_e32 v123, 0xffff0000, v78
	v_lshlrev_b32_e32 v158, 16, v72
	v_and_b32_e32 v159, 0xffff0000, v72
	v_cvt_pk_fp8_f32 v4, v144, v145 op_sel:[0,0,1]
	v_lshlrev_b32_e32 v160, 16, v80
	v_and_b32_e32 v161, 0xffff0000, v80
	s_add_u32 s24, s15, 0x6000
	global_store_dword v[2:3], v4, off offset:1024
	v_mov_b32_e32 v4, 0
	v_cvt_pk_fp8_f32 v4, v146, v147
	s_addc_u32 s25, s17, 0
	v_cvt_pk_fp8_f32 v4, v142, v143 op_sel:[0,0,1]
	global_store_dword v[2:3], v4, off offset:1280
	v_mov_b32_e32 v4, 0
	v_cvt_pk_fp8_f32 v4, v152, v153
	v_cvt_pk_fp8_f32 v4, v150, v151 op_sel:[0,0,1]
	global_store_dword v[2:3], v4, off offset:1536
	v_mov_b32_e32 v4, 0
	v_cvt_pk_fp8_f32 v4, v156, v157
	v_cvt_pk_fp8_f32 v4, v154, v155 op_sel:[0,0,1]
	global_store_dword v[2:3], v4, off offset:1792
	s_add_u32 s100, s15, 0x6000
	s_addc_u32 s101, s17, 0
	s_add_u32 s98, s15, 0x8000
	s_addc_u32 s99, s17, 0
	global_load_dwordx4 v[164:167], v240, s[22:23]
	global_load_dwordx4 v[168:171], v241, s[22:23]
	global_load_dwordx4 v[172:175], v242, s[22:23]
	global_load_dwordx4 v[176:179], v243, s[22:23]
	global_load_dwordx4 v[196:199], v244, s[22:23]
	global_load_dwordx4 v[200:203], v245, s[22:23]
	global_load_dwordx4 v[204:207], v246, s[22:23]
	global_load_dwordx4 v[208:211], v247, s[22:23]
	global_load_dwordx4 v[212:215], v[82:83], off
	global_load_dwordx4 v[216:219], v240, s[100:101]
	global_load_dwordx4 v[220:223], v240, s[98:99]
	global_load_dwordx4 v[224:227], v[82:83], off offset:1024
	global_load_dwordx4 v[228:231], v241, s[100:101]
	global_load_dwordx4 v[232:235], v241, s[98:99]
	global_load_dwordx4 v[236:239], v[82:83], off offset:2048
	global_load_dwordx4 v[252:255], v242, s[100:101]
	v_lshlrev_b32_e32 v2, 16, v50
	v_and_b32_e32 v3, 0xffff0000, v50
	s_waitcnt vmcnt(15)
	v_pk_fma_f32 v[4:5], v[164:165], v[8:9], v[2:3]
	v_lshlrev_b32_e32 v2, 16, v51
	v_and_b32_e32 v3, 0xffff0000, v51
	v_lshlrev_b32_e32 v8, 16, v59
	v_and_b32_e32 v9, 0xffff0000, v59
	v_pk_fma_f32 v[10:11], v[166:167], v[8:9], v[2:3]
	v_cvt_pk_bf16_f32 v2, v4, v5
	v_cvt_pk_bf16_f32 v3, v10, v11
	global_store_dwordx2 v[98:99], v[2:3], off nt
	v_lshlrev_b32_e32 v2, 16, v52
	v_and_b32_e32 v3, 0xffff0000, v52
	v_mov_b32_e32 v100, v11
	s_waitcnt vmcnt(15)
	v_pk_fma_f32 v[2:3], v[168:169], v[12:13], v[2:3]
	v_lshlrev_b32_e32 v6, 16, v53
	v_and_b32_e32 v7, 0xffff0000, v53
	v_lshlrev_b32_e32 v12, 16, v61
	v_and_b32_e32 v13, 0xffff0000, v61
	v_pk_fma_f32 v[6:7], v[170:171], v[12:13], v[6:7]
	v_cvt_pk_bf16_f32 v8, v2, v3
	v_cvt_pk_bf16_f32 v9, v6, v7
	v_mov_b32_e32 v12, v5
	v_mov_b32_e32 v13, v3
	global_store_dwordx2 v[98:99], v[8:9], off offset:512 nt
	v_mov_b32_e32 v8, v4
	v_mov_b32_e32 v9, v2
	v_pk_mul_f32 v[12:13], v[12:13], v[12:13]
	v_mov_b32_e32 v101, v7
	v_pk_fma_f32 v[8:9], v[8:9], v[8:9], v[12:13]
	v_mov_b32_e32 v12, v10
	v_mov_b32_e32 v13, v6
	v_pk_mul_f32 v[100:101], v[100:101], v[100:101]
	s_nop 0
	v_pk_fma_f32 v[12:13], v[12:13], v[12:13], v[100:101]
	v_pk_add_f32 v[8:9], v[8:9], v[12:13]
	v_lshlrev_b32_e32 v12, 16, v62
	v_pk_add_f32 v[104:105], v[8:9], v[8:9] op_sel:[0,1] op_sel_hi:[1,0]
	v_lshlrev_b32_e32 v8, 16, v54
	v_and_b32_e32 v9, 0xffff0000, v54
	v_and_b32_e32 v13, 0xffff0000, v62
	s_waitcnt vmcnt(15)
	v_pk_fma_f32 v[12:13], v[172:173], v[12:13], v[8:9]
	v_lshlrev_b32_e32 v8, 16, v55
	v_and_b32_e32 v9, 0xffff0000, v55
	v_lshlrev_b32_e32 v100, 16, v63
	v_and_b32_e32 v101, 0xffff0000, v63
	v_pk_fma_f32 v[106:107], v[174:175], v[100:101], v[8:9]
	global_load_dwordx4 v[172:175], v242, s[98:99]
	v_cvt_pk_bf16_f32 v8, v12, v13
	v_cvt_pk_bf16_f32 v9, v106, v107
	v_mov_b32_e32 v100, v13
	v_mov_b32_e32 v101, v107
	global_store_dwordx2 v[98:99], v[8:9], off offset:1024 nt
	v_mov_b32_e32 v8, v12
	v_mov_b32_e32 v9, v106
	v_pk_mul_f32 v[100:101], v[100:101], v[100:101]
	s_nop 0
	v_pk_fma_f32 v[8:9], v[8:9], v[8:9], v[100:101]
	v_pk_add_f32 v[108:109], v[8:9], v[8:9] op_sel:[0,1] op_sel_hi:[1,0]
	v_lshlrev_b32_e32 v8, 16, v56
	v_and_b32_e32 v9, 0xffff0000, v56
	s_waitcnt vmcnt(16)
	v_pk_fma_f32 v[110:111], v[176:177], v[110:111], v[8:9]
	v_lshlrev_b32_e32 v8, 16, v57
	v_and_b32_e32 v9, 0xffff0000, v57
	v_lshlrev_b32_e32 v100, 16, v65
	v_and_b32_e32 v101, 0xffff0000, v65
	v_pk_fma_f32 v[112:113], v[178:179], v[100:101], v[8:9]
	global_load_dwordx4 v[176:179], v[82:83], off offset:3072
	v_cvt_pk_bf16_f32 v8, v110, v111
	v_cvt_pk_bf16_f32 v9, v112, v113
	global_store_dwordx2 v[98:99], v[8:9], off offset:1536 nt
	v_mul_f32_e32 v8, v111, v111
	v_pk_fma_f32 v[116:117], v[110:111], v[110:111], v[8:9] op_sel_hi:[1,1,0]
	v_mul_f32_e32 v8, v113, v113
	v_pk_fma_f32 v[118:119], v[112:113], v[112:113], v[8:9] op_sel_hi:[1,1,0]
	v_lshlrev_b32_e32 v8, 16, v66
	v_and_b32_e32 v9, 0xffff0000, v66
	s_waitcnt vmcnt(17)
	v_pk_fma_f32 v[8:9], v[196:197], v[114:115], v[8:9]
	v_lshlrev_b32_e32 v100, 16, v67
	v_and_b32_e32 v101, 0xffff0000, v67
	v_lshlrev_b32_e32 v114, 16, v75
	v_and_b32_e32 v115, 0xffff0000, v75
	v_pk_fma_f32 v[114:115], v[198:199], v[114:115], v[100:101]
	global_load_dwordx4 v[196:199], v243, s[100:101]
	v_cvt_pk_bf16_f32 v100, v8, v9
	v_cvt_pk_bf16_f32 v101, v114, v115
	global_store_dwordx2 v[98:99], v[100:101], off offset:2048 nt
	v_pk_mul_f32 v[100:101], v[8:9], v[8:9]
	v_pk_mul_f32 v[102:103], v[114:115], v[114:115]
	v_mov_b32_e32 v105, v100
	v_mov_b32_e32 v109, v101
	v_mov_b32_e32 v117, v102
	v_mov_b32_e32 v119, v103
	v_pk_add_f32 v[100:101], v[104:105], v[108:109]
	v_pk_add_f32 v[102:103], v[116:117], v[118:119]
	v_lshlrev_b32_e32 v108, 16, v68
	v_pk_add_f32 v[100:101], v[100:101], v[102:103]
	v_and_b32_e32 v109, 0xffff0000, v68
	v_pk_add_f32 v[104:105], v[100:101], v[100:101] op_sel:[0,1] op_sel_hi:[1,0]
	v_lshlrev_b32_e32 v116, 16, v76
	v_and_b32_e32 v117, 0xffff0000, v76
	s_waitcnt vmcnt(18)
	v_pk_fma_f32 v[118:119], v[200:201], v[116:117], v[108:109]
	v_lshlrev_b32_e32 v100, 16, v69
	v_and_b32_e32 v101, 0xffff0000, v69
	v_lshlrev_b32_e32 v108, 16, v77
	v_and_b32_e32 v109, 0xffff0000, v77
	v_pk_fma_f32 v[120:121], v[202:203], v[108:109], v[100:101]
	global_load_dwordx4 v[200:203], v243, s[98:99]
	v_cvt_pk_bf16_f32 v100, v118, v119
	v_cvt_pk_bf16_f32 v101, v120, v121
	v_mov_b32_e32 v102, v119
	v_mov_b32_e32 v103, v121
	global_store_dwordx2 v[98:99], v[100:101], off offset:2560 nt
	v_mov_b32_e32 v100, v118
	v_mov_b32_e32 v101, v120
	v_pk_mul_f32 v[102:103], v[102:103], v[102:103]
	v_lshlrev_b32_e32 v116, 16, v70
	v_pk_fma_f32 v[100:101], v[100:101], v[100:101], v[102:103]
	v_and_b32_e32 v117, 0xffff0000, v70
	v_pk_add_f32 v[108:109], v[100:101], v[100:101] op_sel:[0,1] op_sel_hi:[1,0]
	s_waitcnt vmcnt(19)
	v_pk_fma_f32 v[122:123], v[204:205], v[122:123], v[116:117]
	v_lshlrev_b32_e32 v100, 16, v71
	v_and_b32_e32 v101, 0xffff0000, v71
	v_lshlrev_b32_e32 v116, 16, v79
	v_and_b32_e32 v117, 0xffff0000, v79
	v_pk_fma_f32 v[124:125], v[206:207], v[116:117], v[100:101]
	global_load_dwordx4 v[204:207], v[84:85], off
	v_cvt_pk_bf16_f32 v100, v122, v123
	v_cvt_pk_bf16_f32 v101, v124, v125
	global_store_dwordx2 v[98:99], v[100:101], off offset:3072 nt
	v_mul_f32_e32 v16, v123, v123
	v_pk_fma_f32 v[116:117], v[122:123], v[122:123], v[16:17] op_sel_hi:[1,1,0]
	v_mul_f32_e32 v16, v125, v125
	v_pk_fma_f32 v[162:163], v[124:125], v[124:125], v[16:17] op_sel_hi:[1,1,0]
	s_add_u32 s22, s15, 0x8000
	s_addc_u32 s23, s17, 0
	s_waitcnt vmcnt(20)
	v_pk_fma_f32 v[158:159], v[208:209], v[160:161], v[158:159]
	v_lshlrev_b32_e32 v100, 16, v73
	v_and_b32_e32 v101, 0xffff0000, v73
	v_lshlrev_b32_e32 v160, 16, v81
	v_and_b32_e32 v161, 0xffff0000, v81
	v_pk_fma_f32 v[160:161], v[210:211], v[160:161], v[100:101]
	global_load_dwordx4 v[208:211], v244, s[100:101]
	v_cvt_pk_bf16_f32 v100, v158, v159
	v_cvt_pk_bf16_f32 v101, v160, v161
	global_store_dwordx2 v[98:99], v[100:101], off offset:3584 nt
	v_pk_mul_f32 v[98:99], v[158:159], v[158:159]
	v_pk_mul_f32 v[100:101], v[160:161], v[160:161]
	v_mov_b32_e32 v105, v98
	v_mov_b32_e32 v109, v99
	v_mov_b32_e32 v117, v100
	v_mov_b32_e32 v163, v101
	v_pk_add_f32 v[98:99], v[104:105], v[108:109]
	v_pk_add_f32 v[100:101], v[116:117], v[162:163]
	s_nop 0
	v_pk_add_f32 v[98:99], v[98:99], v[100:101]
	s_nop 0
	v_add_f32_e32 v16, v98, v99
	s_waitcnt lgkmcnt(0)
	s_nop 1
	v_add_f32_dpp v16, v16, v16 quad_perm:[1,0,3,2] row_mask:0xf bank_mask:0xf
	s_nop 1
	v_add_f32_dpp v16, v16, v16 quad_perm:[2,3,0,1] row_mask:0xf bank_mask:0xf
	s_nop 1
	v_add_f32_dpp v16, v16, v16 row_half_mirror row_mask:0xf bank_mask:0xf
	s_nop 1
	v_add_f32_dpp v16, v16, v16 row_mirror row_mask:0xf bank_mask:0xf
	v_mov_b32_e32 v98, v16
	s_nop 1
	v_permlane16_swap_b32 v98, v16
	v_add_f32_e32 v16, v98, v16
	v_mov_b32_e32 v98, v16
	s_nop 1
	v_permlane32_swap_b32 v98, v16
	v_add_f32_e32 v16, v98, v16
	v_fmamk_f32 v16, v16, 0x3a000000, v248
	v_cmp_gt_f32_e32 vcc, s51, v16
	v_mul_f32_e32 v98, 0x4b800000, v16
	s_nop 0
	v_cndmask_b32_e32 v16, v16, v98, vcc
	v_rsq_f32_e32 v16, v16
	s_nop 0
	v_mul_f32_e32 v98, 0x45800000, v16
	v_cndmask_b32_e32 v16, v16, v98, vcc
	v_pk_mul_f32 v[10:11], v[10:11], v[16:17] op_sel_hi:[1,0]
	v_pk_mul_f32 v[4:5], v[4:5], v[16:17] op_sel_hi:[1,0]
	v_pk_mul_f32 v[2:3], v[2:3], v[16:17] op_sel_hi:[1,0]
	v_pk_mul_f32 v[110:111], v[110:111], v[16:17] op_sel_hi:[1,0]
	v_pk_mul_f32 v[8:9], v[8:9], v[16:17] op_sel_hi:[1,0]
	v_pk_mul_f32 v[120:121], v[120:121], v[16:17] op_sel_hi:[1,0]
	v_pk_mul_f32 v[118:119], v[118:119], v[16:17] op_sel_hi:[1,0]
	v_pk_mul_f32 v[124:125], v[124:125], v[16:17] op_sel_hi:[1,0]
	v_pk_mul_f32 v[122:123], v[122:123], v[16:17] op_sel_hi:[1,0]
	v_pk_mul_f32 v[160:161], v[160:161], v[16:17] op_sel_hi:[1,0]
	v_pk_mul_f32 v[158:159], v[158:159], v[16:17] op_sel_hi:[1,0]
	s_waitcnt vmcnt(21)
	v_pk_mul_f32 v[4:5], v[212:213], v[4:5]
	v_pk_mul_f32 v[10:11], v[214:215], v[10:11]
	global_load_dwordx4 v[212:215], v244, s[98:99]
	s_waitcnt vmcnt(20)
	v_pk_add_f32 v[98:99], v[222:223], 1.0 op_sel_hi:[1,0]
	v_pk_add_f32 v[100:101], v[220:221], 1.0 op_sel_hi:[1,0]
	global_load_dwordx4 v[220:223], v[86:87], off
	v_pk_fma_f32 v[98:99], v[98:99], v[10:11], v[218:219]
	v_pk_fma_f32 v[100:101], v[100:101], v[4:5], v[216:217]
	global_load_dwordx4 v[216:219], v245, s[100:101]
	v_max_f32_e64 v4, |v98|, |v99|
	v_max3_f32 v108, |v100|, |v101|, v4
	v_pk_mul_f32 v[4:5], v[6:7], v[16:17] op_sel_hi:[1,0]
	s_waitcnt vmcnt(21)
	v_pk_mul_f32 v[2:3], v[224:225], v[2:3]
	v_pk_mul_f32 v[4:5], v[226:227], v[4:5]
	global_load_dwordx4 v[224:227], v245, s[98:99]
	s_waitcnt vmcnt(20)
	v_pk_add_f32 v[6:7], v[234:235], 1.0 op_sel_hi:[1,0]
	v_pk_add_f32 v[10:11], v[232:233], 1.0 op_sel_hi:[1,0]
	global_load_dwordx4 v[232:235], v[88:89], off
	v_pk_fma_f32 v[102:103], v[6:7], v[4:5], v[230:231]
	v_pk_fma_f32 v[104:105], v[10:11], v[2:3], v[228:229]
	global_load_dwordx4 v[228:231], v246, s[100:101]
	v_max_f32_e64 v2, |v102|, |v103|
	v_max3_f32 v2, |v104|, |v105|, v2
	v_max3_f32 v116, v108, 0, v2
	v_pk_mul_f32 v[6:7], v[106:107], v[16:17] op_sel_hi:[1,0]
	v_pk_mul_f32 v[10:11], v[12:13], v[16:17] op_sel_hi:[1,0]
	s_waitcnt vmcnt(21)
	v_pk_mul_f32 v[4:5], v[238:239], v[6:7]
	v_pk_mul_f32 v[2:3], v[236:237], v[10:11]
	global_load_dwordx4 v[236:239], v246, s[98:99]
	s_waitcnt vmcnt(18)
	v_pk_add_f32 v[6:7], v[174:175], 1.0 op_sel_hi:[1,0]
	v_pk_add_f32 v[10:11], v[172:173], 1.0 op_sel_hi:[1,0]
	global_load_dwordx4 v[172:175], v[90:91], off
	v_pk_fma_f32 v[106:107], v[6:7], v[4:5], v[254:255]
	v_pk_fma_f32 v[108:109], v[10:11], v[2:3], v[252:253]
	global_load_dwordx4 v[252:255], v247, s[100:101]
	v_max_f32_e64 v2, |v106|, |v107|
	v_max3_f32 v117, |v108|, |v109|, v2
	v_pk_mul_f32 v[6:7], v[112:113], v[16:17] op_sel_hi:[1,0]
	s_waitcnt vmcnt(18)
	v_pk_mul_f32 v[2:3], v[176:177], v[110:111]
	v_pk_mul_f32 v[4:5], v[178:179], v[6:7]
	global_load_dwordx4 v[176:179], v247, s[98:99]
	s_waitcnt vmcnt(15)
	v_pk_add_f32 v[6:7], v[202:203], 1.0 op_sel_hi:[1,0]
	v_pk_add_f32 v[112:113], v[200:201], 1.0 op_sel_hi:[1,0]
	v_pk_fma_f32 v[110:111], v[6:7], v[4:5], v[198:199]
	v_pk_fma_f32 v[112:113], v[112:113], v[2:3], v[196:197]
	v_max_f32_e64 v2, |v110|, |v111|
	v_max3_f32 v2, |v112|, |v113|, v2
	v_max3_f32 v166, v116, v117, v2
	v_pk_mul_f32 v[6:7], v[114:115], v[16:17] op_sel_hi:[1,0]
	s_waitcnt vmcnt(13)
	v_pk_mul_f32 v[2:3], v[204:205], v[8:9]
	v_pk_mul_f32 v[4:5], v[206:207], v[6:7]
	s_waitcnt vmcnt(9)
	v_pk_add_f32 v[6:7], v[214:215], 1.0 op_sel_hi:[1,0]
	v_pk_add_f32 v[8:9], v[212:213], 1.0 op_sel_hi:[1,0]
	v_pk_fma_f32 v[114:115], v[6:7], v[4:5], v[210:211]
	v_pk_fma_f32 v[116:117], v[8:9], v[2:3], v[208:209]
	v_max_f32_e64 v2, |v114|, |v115|
	v_max3_f32 v162, |v116|, |v117|, v2
	s_waitcnt vmcnt(8)
	v_pk_mul_f32 v[4:5], v[120:121], v[222:223]
	v_pk_mul_f32 v[2:3], v[118:119], v[220:221]
	s_waitcnt vmcnt(6)
	v_pk_add_f32 v[12:13], v[226:227], 1.0 op_sel_hi:[1,0]
	v_pk_add_f32 v[10:11], v[224:225], 1.0 op_sel_hi:[1,0]
	v_pk_fma_f32 v[118:119], v[4:5], v[12:13], v[218:219]
	v_pk_fma_f32 v[120:121], v[2:3], v[10:11], v[216:217]
	v_max_f32_e64 v2, |v118|, |v119|
	v_max3_f32 v2, |v120|, |v121|, v2
	v_max3_f32 v162, v166, v162, v2
	s_waitcnt vmcnt(5)
	v_pk_mul_f32 v[4:5], v[124:125], v[234:235]
	v_pk_mul_f32 v[2:3], v[122:123], v[232:233]
	s_waitcnt vmcnt(3)
	v_pk_add_f32 v[12:13], v[238:239], 1.0 op_sel_hi:[1,0]
	v_pk_add_f32 v[10:11], v[236:237], 1.0 op_sel_hi:[1,0]
	v_pk_fma_f32 v[122:123], v[4:5], v[12:13], v[230:231]
	v_pk_fma_f32 v[124:125], v[2:3], v[10:11], v[228:229]
	v_max_f32_e64 v2, |v122|, |v123|
	v_max3_f32 v163, |v124|, |v125|, v2
	s_waitcnt vmcnt(2)
	v_pk_mul_f32 v[8:9], v[160:161], v[174:175]
	v_pk_mul_f32 v[6:7], v[158:159], v[172:173]
	s_waitcnt vmcnt(0)
	v_pk_add_f32 v[12:13], v[178:179], 1.0 op_sel_hi:[1,0]
	v_pk_add_f32 v[10:11], v[176:177], 1.0 op_sel_hi:[1,0]
	v_pk_fma_f32 v[4:5], v[8:9], v[12:13], v[254:255]
	v_pk_fma_f32 v[2:3], v[6:7], v[10:11], v[252:253]
	v_max_f32_e64 v6, |v4|, |v5|
	v_max3_f32 v6, |v2|, |v3|, v6
	v_max3_f32 v6, v162, v163, v6
	s_waitcnt lgkmcnt(0)
	s_nop 1
	v_max_f32_dpp v6, v6, v6 quad_perm:[1,0,3,2] row_mask:0xf bank_mask:0xf
	s_nop 1
	v_max_f32_dpp v6, v6, v6 quad_perm:[2,3,0,1] row_mask:0xf bank_mask:0xf
	s_nop 1
	v_max_f32_dpp v6, v6, v6 row_half_mirror row_mask:0xf bank_mask:0xf
	s_nop 1
	v_max_f32_dpp v6, v6, v6 row_mirror row_mask:0xf bank_mask:0xf
	v_mov_b32_e32 v7, v6
	s_nop 1
	v_permlane16_swap_b32 v7, v6
	v_max_f32_e32 v6, v7, v6
	ds_bpermute_b32 v7, v183, v6
	s_and_saveexec_b64 s[22:23], s[4:5]
	s_cbranch_execz .LBB0_1697
	s_waitcnt lgkmcnt(0)
	v_max_f32_e32 v7, v7, v7
	v_max_f32_e32 v6, v6, v6
	s_lshl_b64 s[24:25], s[18:19], 2
	v_max_f32_e32 v6, v6, v7
	s_add_u32 s24, s35, s24
	v_mul_f32_e32 v6, 0x3c010204, v6
	s_addc_u32 s25, s38, s25
	global_store_dword v17, v6, s[24:25]

.LBB0_3197:
	s_add_i32 s14, s29, s47
	s_add_i32 s16, s14, -8
	s_min_i32 s15, s16, 0x4000
	s_ashr_i32 s15, s15, 13
	s_mul_i32 s18, s15, 0x3000
	s_ashr_i32 s17, s16, 31
	s_ashr_i32 s19, s18, 31
	s_lshl_b64 s[22:23], s[16:17], 11
	s_lshl_b64 s[18:19], s[18:19], 2
	s_add_u32 s15, s33, s18
	s_addc_u32 s26, s34, s19
	s_add_u32 s18, s15, 0x4000
	s_addc_u32 s19, s26, 0
	s_waitcnt lgkmcnt(0)
	s_add_u32 s100, s15, 0x6000
	s_addc_u32 s101, s26, 0
	s_add_u32 s98, s15, 0x8000
	s_addc_u32 s99, s26, 0
	global_load_dwordx4 v[140:143], v240, s[18:19]
	global_load_dwordx4 v[144:147], v241, s[18:19]
	global_load_dwordx4 v[148:151], v242, s[18:19]
	global_load_dwordx4 v[152:155], v243, s[18:19]
	global_load_dwordx4 v[156:159], v244, s[18:19]
	global_load_dwordx4 v[160:163], v245, s[18:19]
	global_load_dwordx4 v[164:167], v246, s[18:19]
	global_load_dwordx4 v[168:171], v247, s[18:19]
	global_load_dwordx4 v[172:175], v[82:83], off
	global_load_dwordx4 v[176:179], v240, s[100:101]
	global_load_dwordx4 v[180:183], v240, s[98:99]
	global_load_dwordx4 v[200:203], v[84:85], off
	global_load_dwordx4 v[204:207], v241, s[100:101]
	global_load_dwordx4 v[208:211], v241, s[98:99]
	global_load_dwordx4 v[212:215], v[86:87], off
	global_load_dwordx4 v[216:219], v242, s[100:101]
	global_load_dwordx4 v[220:223], v242, s[98:99]
	global_load_dwordx4 v[224:227], v[88:89], off
	global_load_dwordx4 v[228:231], v243, s[100:101]
	global_load_dwordx4 v[232:235], v243, s[98:99]
	global_load_dwordx4 v[236:239], v[90:91], off
	global_load_dwordx4 v[252:255], v244, s[100:101]
	s_waitcnt vmcnt(32)
	v_lshlrev_b32_e32 v2, 16, v18
	v_and_b32_e32 v3, 0xffff0000, v18
	s_waitcnt vmcnt(28)
	v_lshlrev_b32_e32 v8, 16, v26
	v_and_b32_e32 v9, 0xffff0000, v26
	s_lshl_b64 s[24:25], s[16:17], 12
	v_lshl_add_u64 v[108:109], v[98:99], 0, s[24:25]
	s_waitcnt vmcnt(27)
	v_lshlrev_b32_e32 v12, 16, v28
	v_and_b32_e32 v13, 0xffff0000, v28
	s_waitcnt vmcnt(25)
	v_lshlrev_b32_e32 v112, 16, v32
	v_and_b32_e32 v113, 0xffff0000, v32
	s_waitcnt vmcnt(20)
	v_lshlrev_b32_e32 v116, 16, v42
	v_and_b32_e32 v117, 0xffff0000, v42
	v_lshlrev_b32_e32 v134, 16, v40
	v_and_b32_e32 v135, 0xffff0000, v40
	s_waitcnt vmcnt(17)
	v_lshlrev_b32_e32 v136, 16, v48
	v_and_b32_e32 v137, 0xffff0000, v48
	s_add_u32 s24, s15, 0x6000
	s_addc_u32 s25, s26, 0
	s_waitcnt vmcnt(21)
	v_pk_fma_f32 v[4:5], v[140:141], v[8:9], v[2:3]
	v_lshlrev_b32_e32 v2, 16, v19
	v_and_b32_e32 v3, 0xffff0000, v19
	v_lshlrev_b32_e32 v8, 16, v27
	v_and_b32_e32 v9, 0xffff0000, v27
	v_pk_fma_f32 v[10:11], v[142:143], v[8:9], v[2:3]
	v_cvt_pk_bf16_f32 v2, v4, v5
	v_cvt_pk_bf16_f32 v3, v10, v11
	global_store_dwordx2 v[108:109], v[2:3], off nt
	v_lshlrev_b32_e32 v2, 16, v20
	v_and_b32_e32 v3, 0xffff0000, v20
	v_mov_b32_e32 v104, v11
	s_waitcnt vmcnt(21)
	v_pk_fma_f32 v[2:3], v[144:145], v[12:13], v[2:3]
	v_lshlrev_b32_e32 v6, 16, v21
	v_and_b32_e32 v7, 0xffff0000, v21
	v_lshlrev_b32_e32 v12, 16, v29
	v_and_b32_e32 v13, 0xffff0000, v29
	v_pk_fma_f32 v[6:7], v[146:147], v[12:13], v[6:7]
	v_cvt_pk_bf16_f32 v8, v2, v3
	v_cvt_pk_bf16_f32 v9, v6, v7
	v_mov_b32_e32 v12, v5
	v_mov_b32_e32 v13, v3
	global_store_dwordx2 v[108:109], v[8:9], off offset:512 nt
	v_mov_b32_e32 v8, v4
	v_mov_b32_e32 v9, v2
	v_pk_mul_f32 v[12:13], v[12:13], v[12:13]
	v_mov_b32_e32 v105, v7
	v_pk_fma_f32 v[8:9], v[8:9], v[8:9], v[12:13]
	v_mov_b32_e32 v12, v10
	v_mov_b32_e32 v13, v6
	v_pk_mul_f32 v[104:105], v[104:105], v[104:105]
	s_nop 0
	v_pk_fma_f32 v[12:13], v[12:13], v[12:13], v[104:105]
	v_pk_add_f32 v[8:9], v[8:9], v[12:13]
	v_lshlrev_b32_e32 v12, 16, v30
	v_pk_add_f32 v[110:111], v[8:9], v[8:9] op_sel:[0,1] op_sel_hi:[1,0]
	v_lshlrev_b32_e32 v8, 16, v22
	v_and_b32_e32 v9, 0xffff0000, v22
	v_and_b32_e32 v13, 0xffff0000, v30
	s_waitcnt vmcnt(21)
	v_pk_fma_f32 v[12:13], v[148:149], v[12:13], v[8:9]
	v_lshlrev_b32_e32 v8, 16, v23
	v_and_b32_e32 v9, 0xffff0000, v23
	v_lshlrev_b32_e32 v104, 16, v31
	v_and_b32_e32 v105, 0xffff0000, v31
	v_pk_fma_f32 v[118:119], v[150:151], v[104:105], v[8:9]
	v_cvt_pk_bf16_f32 v8, v12, v13
	v_cvt_pk_bf16_f32 v9, v118, v119
	v_mov_b32_e32 v104, v13
	v_mov_b32_e32 v105, v119
	global_store_dwordx2 v[108:109], v[8:9], off offset:1024 nt
	v_mov_b32_e32 v8, v12
	v_mov_b32_e32 v9, v118
	v_pk_mul_f32 v[104:105], v[104:105], v[104:105]
	s_nop 0
	v_pk_fma_f32 v[8:9], v[8:9], v[8:9], v[104:105]
	v_pk_add_f32 v[114:115], v[8:9], v[8:9] op_sel:[0,1] op_sel_hi:[1,0]
	v_lshlrev_b32_e32 v8, 16, v24
	v_and_b32_e32 v9, 0xffff0000, v24
	s_waitcnt vmcnt(21)
	v_pk_fma_f32 v[112:113], v[152:153], v[112:113], v[8:9]
	v_lshlrev_b32_e32 v8, 16, v25
	v_and_b32_e32 v9, 0xffff0000, v25
	v_lshlrev_b32_e32 v104, 16, v33
	v_and_b32_e32 v105, 0xffff0000, v33
	v_pk_fma_f32 v[122:123], v[154:155], v[104:105], v[8:9]
	v_cvt_pk_bf16_f32 v8, v112, v113
	v_cvt_pk_bf16_f32 v9, v122, v123
	global_store_dwordx2 v[108:109], v[8:9], off offset:1536 nt
	v_mul_f32_e32 v8, v113, v113
	v_pk_fma_f32 v[120:121], v[112:113], v[112:113], v[8:9] op_sel_hi:[1,1,0]
	v_mul_f32_e32 v8, v123, v123
	v_pk_fma_f32 v[124:125], v[122:123], v[122:123], v[8:9] op_sel_hi:[1,1,0]
	v_lshlrev_b32_e32 v8, 16, v34
	v_and_b32_e32 v9, 0xffff0000, v34
	s_waitcnt vmcnt(21)
	v_pk_fma_f32 v[8:9], v[156:157], v[116:117], v[8:9]
	v_lshlrev_b32_e32 v104, 16, v35
	v_and_b32_e32 v105, 0xffff0000, v35
	v_lshlrev_b32_e32 v116, 16, v43
	v_and_b32_e32 v117, 0xffff0000, v43
	v_pk_fma_f32 v[116:117], v[158:159], v[116:117], v[104:105]
	v_cvt_pk_bf16_f32 v104, v8, v9
	v_cvt_pk_bf16_f32 v105, v116, v117
	global_store_dwordx2 v[108:109], v[104:105], off offset:2048 nt
	v_pk_mul_f32 v[104:105], v[8:9], v[8:9]
	v_pk_mul_f32 v[106:107], v[116:117], v[116:117]
	v_mov_b32_e32 v111, v104
	v_mov_b32_e32 v115, v105
	v_mov_b32_e32 v121, v106
	v_mov_b32_e32 v125, v107
	v_pk_add_f32 v[104:105], v[110:111], v[114:115]
	v_pk_add_f32 v[106:107], v[120:121], v[124:125]
	v_lshlrev_b32_e32 v110, 16, v36
	v_pk_add_f32 v[104:105], v[104:105], v[106:107]
	v_and_b32_e32 v111, 0xffff0000, v36
	v_pk_add_f32 v[126:127], v[104:105], v[104:105] op_sel:[0,1] op_sel_hi:[1,0]
	v_lshlrev_b32_e32 v114, 16, v44
	v_and_b32_e32 v115, 0xffff0000, v44
	v_lshlrev_b32_e32 v120, 16, v46
	v_and_b32_e32 v121, 0xffff0000, v46
	s_waitcnt vmcnt(21)
	v_pk_fma_f32 v[114:115], v[160:161], v[114:115], v[110:111]
	v_lshlrev_b32_e32 v104, 16, v37
	v_and_b32_e32 v105, 0xffff0000, v37
	v_lshlrev_b32_e32 v110, 16, v45
	v_and_b32_e32 v111, 0xffff0000, v45
	v_pk_fma_f32 v[124:125], v[162:163], v[110:111], v[104:105]
	v_cvt_pk_bf16_f32 v104, v114, v115
	v_cvt_pk_bf16_f32 v105, v124, v125
	v_mov_b32_e32 v106, v115
	v_mov_b32_e32 v107, v125
	global_store_dwordx2 v[108:109], v[104:105], off offset:2560 nt
	v_mov_b32_e32 v104, v114
	v_mov_b32_e32 v105, v124
	v_pk_mul_f32 v[106:107], v[106:107], v[106:107]
	v_lshlrev_b32_e32 v110, 16, v38
	v_pk_fma_f32 v[104:105], v[104:105], v[104:105], v[106:107]
	v_and_b32_e32 v111, 0xffff0000, v38
	v_pk_add_f32 v[128:129], v[104:105], v[104:105] op_sel:[0,1] op_sel_hi:[1,0]
	s_waitcnt vmcnt(21)
	v_pk_fma_f32 v[110:111], v[164:165], v[120:121], v[110:111]
	v_lshlrev_b32_e32 v104, 16, v39
	v_and_b32_e32 v105, 0xffff0000, v39
	v_lshlrev_b32_e32 v120, 16, v47
	v_and_b32_e32 v121, 0xffff0000, v47
	v_pk_fma_f32 v[120:121], v[166:167], v[120:121], v[104:105]
	global_load_dwordx4 v[164:167], v244, s[98:99]
	v_cvt_pk_bf16_f32 v104, v110, v111
	v_cvt_pk_bf16_f32 v105, v120, v121
	global_store_dwordx2 v[108:109], v[104:105], off offset:3072 nt
	v_mul_f32_e32 v104, v111, v111
	v_pk_fma_f32 v[130:131], v[110:111], v[110:111], v[104:105] op_sel_hi:[1,1,0]
	v_mul_f32_e32 v104, v121, v121
	v_pk_fma_f32 v[132:133], v[120:121], v[120:121], v[104:105] op_sel_hi:[1,1,0]
	s_add_u32 s18, s15, 0x8000
	s_addc_u32 s19, s26, 0
	s_waitcnt vmcnt(22)
	v_pk_fma_f32 v[104:105], v[168:169], v[136:137], v[134:135]
	v_lshlrev_b32_e32 v134, 16, v41
	v_and_b32_e32 v135, 0xffff0000, v41
	v_lshlrev_b32_e32 v136, 16, v49
	v_and_b32_e32 v137, 0xffff0000, v49
	v_pk_fma_f32 v[106:107], v[170:171], v[136:137], v[134:135]
	global_load_dwordx4 v[168:171], v[92:93], off
	v_cvt_pk_bf16_f32 v134, v104, v105
	v_cvt_pk_bf16_f32 v135, v106, v107
	global_store_dwordx2 v[108:109], v[134:135], off offset:3584 nt
	v_pk_mul_f32 v[108:109], v[104:105], v[104:105]
	v_pk_mul_f32 v[134:135], v[106:107], v[106:107]
	v_mov_b32_e32 v127, v108
	v_mov_b32_e32 v129, v109
	v_mov_b32_e32 v131, v134
	v_mov_b32_e32 v133, v135
	v_pk_add_f32 v[108:109], v[126:127], v[128:129]
	v_pk_add_f32 v[126:127], v[130:131], v[132:133]
	s_nop 0
	v_pk_add_f32 v[108:109], v[108:109], v[126:127]
	v_add_f32_e32 v108, v108, v109
	s_waitcnt lgkmcnt(0)
	s_nop 1
	v_add_f32_dpp v108, v108, v108 quad_perm:[1,0,3,2] row_mask:0xf bank_mask:0xf
	s_nop 1
	v_add_f32_dpp v108, v108, v108 quad_perm:[2,3,0,1] row_mask:0xf bank_mask:0xf
	s_nop 1
	v_add_f32_dpp v108, v108, v108 row_half_mirror row_mask:0xf bank_mask:0xf
	s_nop 1
	v_add_f32_dpp v108, v108, v108 row_mirror row_mask:0xf bank_mask:0xf
	v_mov_b32_e32 v109, v108
	s_nop 1
	v_permlane16_swap_b32 v109, v108
	v_add_f32_e32 v108, v109, v108
	v_mov_b32_e32 v109, v108
	s_nop 1
	v_permlane32_swap_b32 v109, v108
	v_add_f32_e32 v108, v109, v108
	v_fmamk_f32 v108, v108, 0x3a000000, v248
	v_cmp_gt_f32_e32 vcc, s51, v108
	v_mul_f32_e32 v109, 0x4b800000, v108
	s_nop 0
	v_cndmask_b32_e32 v108, v108, v109, vcc
	v_rsq_f32_e32 v108, v108
	s_nop 0
	v_mul_f32_e32 v109, 0x45800000, v108
	v_cndmask_b32_e32 v108, v108, v109, vcc
	v_pk_mul_f32 v[10:11], v[10:11], v[108:109] op_sel_hi:[1,0]
	v_pk_mul_f32 v[4:5], v[4:5], v[108:109] op_sel_hi:[1,0]
	s_waitcnt vmcnt(23)
	v_pk_mul_f32 v[10:11], v[174:175], v[10:11]
	v_pk_mul_f32 v[4:5], v[172:173], v[4:5]
	global_load_dwordx4 v[172:175], v245, s[100:101]
	s_waitcnt vmcnt(22)
	v_pk_add_f32 v[126:127], v[182:183], 1.0 op_sel_hi:[1,0]
	v_pk_add_f32 v[128:129], v[180:181], 1.0 op_sel_hi:[1,0]
	global_load_dwordx4 v[180:183], v245, s[98:99]
	v_pk_fma_f32 v[134:135], v[126:127], v[10:11], v[178:179]
	v_pk_fma_f32 v[132:133], v[128:129], v[4:5], v[176:177]
	global_load_dwordx4 v[176:179], v[94:95], off
	v_max_f32_e64 v4, |v134|, |v135|
	v_max3_f32 v109, |v132|, |v133|, v4
	v_pk_mul_f32 v[4:5], v[6:7], v[108:109] op_sel_hi:[1,0]
	v_pk_mul_f32 v[2:3], v[2:3], v[108:109] op_sel_hi:[1,0]
	s_waitcnt vmcnt(23)
	v_pk_mul_f32 v[4:5], v[202:203], v[4:5]
	v_pk_mul_f32 v[2:3], v[200:201], v[2:3]
	global_load_dwordx4 v[200:203], v246, s[100:101]
	s_waitcnt vmcnt(22)
	v_pk_add_f32 v[6:7], v[210:211], 1.0 op_sel_hi:[1,0]
	v_pk_add_f32 v[10:11], v[208:209], 1.0 op_sel_hi:[1,0]
	global_load_dwordx4 v[208:211], v246, s[98:99]
	v_pk_fma_f32 v[138:139], v[6:7], v[4:5], v[206:207]
	v_pk_fma_f32 v[136:137], v[10:11], v[2:3], v[204:205]
	global_load_dwordx4 v[204:207], v[96:97], off
	v_max_f32_e64 v2, |v138|, |v139|
	v_max3_f32 v2, |v136|, |v137|, v2
	v_max3_f32 v109, v109, 0, v2
	v_pk_mul_f32 v[6:7], v[118:119], v[108:109] op_sel_hi:[1,0]
	v_pk_mul_f32 v[10:11], v[12:13], v[108:109] op_sel_hi:[1,0]
	v_pk_mul_f32 v[112:113], v[112:113], v[108:109] op_sel_hi:[1,0]
	s_waitcnt vmcnt(23)
	v_pk_mul_f32 v[4:5], v[214:215], v[6:7]
	v_pk_mul_f32 v[2:3], v[212:213], v[10:11]
	global_load_dwordx4 v[212:215], v247, s[100:101]
	s_waitcnt vmcnt(22)
	v_pk_add_f32 v[6:7], v[222:223], 1.0 op_sel_hi:[1,0]
	v_pk_add_f32 v[10:11], v[220:221], 1.0 op_sel_hi:[1,0]
	global_load_dwordx4 v[220:223], v247, s[98:99]
	v_pk_fma_f32 v[142:143], v[6:7], v[4:5], v[218:219]
	v_pk_fma_f32 v[140:141], v[10:11], v[2:3], v[216:217]
	v_max_f32_e64 v2, |v142|, |v143|
	v_max3_f32 v118, |v140|, |v141|, v2
	v_pk_mul_f32 v[6:7], v[122:123], v[108:109] op_sel_hi:[1,0]
	s_waitcnt vmcnt(22)
	v_pk_mul_f32 v[2:3], v[224:225], v[112:113]
	v_pk_mul_f32 v[4:5], v[226:227], v[6:7]
	s_waitcnt vmcnt(20)
	v_pk_add_f32 v[6:7], v[234:235], 1.0 op_sel_hi:[1,0]
	v_pk_add_f32 v[112:113], v[232:233], 1.0 op_sel_hi:[1,0]
	v_pk_fma_f32 v[146:147], v[6:7], v[4:5], v[230:231]
	v_pk_fma_f32 v[144:145], v[112:113], v[2:3], v[228:229]
	v_max_f32_e64 v2, |v146|, |v147|
	v_max3_f32 v2, |v144|, |v145|, v2
	v_max3_f32 v109, v109, v118, v2
	v_pk_mul_f32 v[6:7], v[116:117], v[108:109] op_sel_hi:[1,0]
	v_pk_mul_f32 v[8:9], v[8:9], v[108:109] op_sel_hi:[1,0]
	v_pk_mul_f32 v[112:113], v[124:125], v[108:109] op_sel_hi:[1,0]
	v_pk_mul_f32 v[114:115], v[114:115], v[108:109] op_sel_hi:[1,0]
	s_waitcnt vmcnt(19)
	v_pk_mul_f32 v[4:5], v[238:239], v[6:7]
	v_pk_mul_f32 v[2:3], v[236:237], v[8:9]
	s_waitcnt vmcnt(11)
	v_pk_add_f32 v[6:7], v[166:167], 1.0 op_sel_hi:[1,0]
	v_pk_add_f32 v[8:9], v[164:165], 1.0 op_sel_hi:[1,0]
	v_pk_fma_f32 v[150:151], v[4:5], v[6:7], v[254:255]
	v_pk_fma_f32 v[148:149], v[2:3], v[8:9], v[252:253]
	v_max_f32_e64 v2, |v150|, |v151|
	v_max3_f32 v116, |v148|, |v149|, v2
	s_waitcnt vmcnt(9)
	v_pk_mul_f32 v[4:5], v[112:113], v[170:171]
	v_pk_mul_f32 v[2:3], v[114:115], v[168:169]
	s_waitcnt vmcnt(6)
	v_pk_add_f32 v[12:13], v[182:183], 1.0 op_sel_hi:[1,0]
	v_pk_add_f32 v[10:11], v[180:181], 1.0 op_sel_hi:[1,0]
	v_pk_fma_f32 v[154:155], v[4:5], v[12:13], v[174:175]
	v_pk_fma_f32 v[152:153], v[2:3], v[10:11], v[172:173]
	v_max_f32_e64 v2, |v154|, |v155|
	v_max3_f32 v2, |v152|, |v153|, v2
	v_max3_f32 v109, v109, v116, v2
	v_pk_mul_f32 v[112:113], v[120:121], v[108:109] op_sel_hi:[1,0]
	v_pk_mul_f32 v[110:111], v[110:111], v[108:109] op_sel_hi:[1,0]
	v_pk_mul_f32 v[106:107], v[106:107], v[108:109] op_sel_hi:[1,0]
	v_pk_mul_f32 v[104:105], v[104:105], v[108:109] op_sel_hi:[1,0]
	s_waitcnt vmcnt(5)
	v_pk_mul_f32 v[4:5], v[112:113], v[178:179]
	v_pk_mul_f32 v[2:3], v[110:111], v[176:177]
	s_waitcnt vmcnt(3)
	v_pk_add_f32 v[12:13], v[210:211], 1.0 op_sel_hi:[1,0]
	v_pk_add_f32 v[10:11], v[208:209], 1.0 op_sel_hi:[1,0]
	v_pk_fma_f32 v[158:159], v[4:5], v[12:13], v[202:203]
	v_pk_fma_f32 v[156:157], v[2:3], v[10:11], v[200:201]
	v_max_f32_e64 v2, |v158|, |v159|
	v_max3_f32 v110, |v156|, |v157|, v2
	s_waitcnt vmcnt(2)
	v_pk_mul_f32 v[8:9], v[106:107], v[206:207]
	v_pk_mul_f32 v[6:7], v[104:105], v[204:205]
	s_waitcnt vmcnt(0)
	v_pk_add_f32 v[12:13], v[222:223], 1.0 op_sel_hi:[1,0]
	v_pk_add_f32 v[10:11], v[220:221], 1.0 op_sel_hi:[1,0]
	v_pk_fma_f32 v[162:163], v[8:9], v[12:13], v[214:215]
	v_pk_fma_f32 v[160:161], v[6:7], v[10:11], v[212:213]
	v_max_f32_e64 v2, |v162|, |v163|
	v_max3_f32 v2, |v160|, |v161|, v2
	v_max3_f32 v2, v109, v110, v2
	s_waitcnt lgkmcnt(0)
	s_nop 1
	v_max_f32_dpp v2, v2, v2 quad_perm:[1,0,3,2] row_mask:0xf bank_mask:0xf
	s_nop 1
	v_max_f32_dpp v2, v2, v2 quad_perm:[2,3,0,1] row_mask:0xf bank_mask:0xf
	s_nop 1
	v_max_f32_dpp v2, v2, v2 row_half_mirror row_mask:0xf bank_mask:0xf
	s_nop 1
	v_max_f32_dpp v2, v2, v2 row_mirror row_mask:0xf bank_mask:0xf
	v_mov_b32_e32 v3, v2
	s_nop 1
	v_permlane16_swap_b32 v3, v2
	v_max_f32_e32 v2, v3, v2
	ds_bpermute_b32 v3, v189, v2
	s_and_saveexec_b64 s[18:19], s[4:5]
	s_cbranch_execz .LBB0_3199
	s_waitcnt lgkmcnt(0)
	v_max_f32_e32 v3, v3, v3
	v_max_f32_e32 v2, v2, v2
	s_lshl_b64 s[16:17], s[16:17], 2
	v_max_f32_e32 v2, v2, v3
	s_add_u32 s16, s35, s16
	v_mul_f32_e32 v2, 0x3c010204, v2
	s_addc_u32 s17, s38, s17
	global_store_dword v17, v2, s[16:17]
.LBB0_3199:
	s_or_b64 exec, exec, s[18:19]
	v_mov_b32_e32 v4, 0
	v_cvt_pk_fp8_f32 v4, v132, v133
	s_waitcnt lgkmcnt(0)
	v_lshl_add_u64 v[2:3], v[100:101], 0, s[22:23]
	s_add_i32 s16, s50, s47
	s_add_i32 s18, s16, -8
	v_cvt_pk_fp8_f32 v4, v134, v135 op_sel:[0,0,1]
	s_min_i32 s15, s18, 0x4000
	s_ashr_i32 s15, s15, 13
	s_mul_i32 s22, s15, 0x3000
	global_store_dword v[2:3], v4, off
	v_mov_b32_e32 v4, 0
	v_cvt_pk_fp8_f32 v4, v136, v137
	s_ashr_i32 s23, s22, 31
	s_ashr_i32 s19, s18, 31
	s_lshl_b64 s[22:23], s[22:23], 2
	v_cvt_pk_fp8_f32 v4, v138, v139 op_sel:[0,0,1]
	s_add_u32 s15, s33, s22
	s_addc_u32 s17, s34, s23
	s_add_u32 s22, s15, 0x4000
	global_store_dword v[2:3], v4, off offset:256
	v_mov_b32_e32 v4, 0
	v_cvt_pk_fp8_f32 v4, v140, v141
	s_addc_u32 s23, s17, 0
	v_lshlrev_b32_e32 v8, 16, v58
	v_and_b32_e32 v9, 0xffff0000, v58
	v_cvt_pk_fp8_f32 v4, v142, v143 op_sel:[0,0,1]
	s_lshl_b64 s[24:25], s[18:19], 12
	v_lshl_add_u64 v[104:105], v[98:99], 0, s[24:25]
	v_lshlrev_b32_e32 v12, 16, v60
	global_store_dword v[2:3], v4, off offset:512
	v_mov_b32_e32 v4, 0
	v_cvt_pk_fp8_f32 v4, v144, v145
	v_and_b32_e32 v13, 0xffff0000, v60
	v_lshlrev_b32_e32 v116, 16, v64
	v_and_b32_e32 v117, 0xffff0000, v64
	v_cvt_pk_fp8_f32 v4, v146, v147 op_sel:[0,0,1]
	v_lshlrev_b32_e32 v120, 16, v74
	v_and_b32_e32 v121, 0xffff0000, v74
	v_lshlrev_b32_e32 v128, 16, v78
	global_store_dword v[2:3], v4, off offset:768
	v_mov_b32_e32 v4, 0
	v_cvt_pk_fp8_f32 v4, v148, v149
	v_and_b32_e32 v129, 0xffff0000, v78
	v_lshlrev_b32_e32 v164, 16, v72
	v_and_b32_e32 v165, 0xffff0000, v72
	v_cvt_pk_fp8_f32 v4, v150, v151 op_sel:[0,0,1]
	v_lshlrev_b32_e32 v166, 16, v80
	v_and_b32_e32 v167, 0xffff0000, v80
	s_add_u32 s24, s15, 0x6000
	global_store_dword v[2:3], v4, off offset:1024
	v_mov_b32_e32 v4, 0
	v_cvt_pk_fp8_f32 v4, v152, v153
	s_addc_u32 s25, s17, 0
	v_cvt_pk_fp8_f32 v4, v154, v155 op_sel:[0,0,1]
	global_store_dword v[2:3], v4, off offset:1280
	v_mov_b32_e32 v4, 0
	v_cvt_pk_fp8_f32 v4, v156, v157
	v_cvt_pk_fp8_f32 v4, v158, v159 op_sel:[0,0,1]
	global_store_dword v[2:3], v4, off offset:1536
	v_mov_b32_e32 v4, 0
	v_cvt_pk_fp8_f32 v4, v160, v161
	v_cvt_pk_fp8_f32 v4, v162, v163 op_sel:[0,0,1]
	global_store_dword v[2:3], v4, off offset:1792
	s_add_u32 s100, s15, 0x6000
	s_addc_u32 s101, s17, 0
	s_add_u32 s98, s15, 0x8000
	s_addc_u32 s99, s17, 0
	global_load_dwordx4 v[172:175], v240, s[22:23]
	global_load_dwordx4 v[176:179], v241, s[22:23]
	global_load_dwordx4 v[180:183], v242, s[22:23]
	global_load_dwordx4 v[200:203], v243, s[22:23]
	global_load_dwordx4 v[204:207], v244, s[22:23]
	global_load_dwordx4 v[208:211], v245, s[22:23]
	global_load_dwordx4 v[212:215], v246, s[22:23]
	global_load_dwordx4 v[216:219], v247, s[22:23]
	global_load_dwordx4 v[220:223], v[82:83], off
	global_load_dwordx4 v[224:227], v240, s[100:101]
	global_load_dwordx4 v[228:231], v240, s[98:99]
	global_load_dwordx4 v[232:235], v[84:85], off
	global_load_dwordx4 v[236:239], v241, s[100:101]
	global_load_dwordx4 v[252:255], v241, s[98:99]
	v_lshlrev_b32_e32 v2, 16, v50
	v_and_b32_e32 v3, 0xffff0000, v50
	s_waitcnt vmcnt(13)
	v_pk_fma_f32 v[4:5], v[172:173], v[8:9], v[2:3]
	v_lshlrev_b32_e32 v2, 16, v51
	v_and_b32_e32 v3, 0xffff0000, v51
	v_lshlrev_b32_e32 v8, 16, v59
	v_and_b32_e32 v9, 0xffff0000, v59
	v_pk_fma_f32 v[10:11], v[174:175], v[8:9], v[2:3]
	v_cvt_pk_bf16_f32 v2, v4, v5
	v_cvt_pk_bf16_f32 v3, v10, v11
	global_store_dwordx2 v[104:105], v[2:3], off nt
	v_lshlrev_b32_e32 v2, 16, v52
	v_and_b32_e32 v3, 0xffff0000, v52
	v_mov_b32_e32 v106, v11
	s_waitcnt vmcnt(13)
	v_pk_fma_f32 v[2:3], v[176:177], v[12:13], v[2:3]
	v_lshlrev_b32_e32 v6, 16, v53
	v_and_b32_e32 v7, 0xffff0000, v53
	v_lshlrev_b32_e32 v12, 16, v61
	v_and_b32_e32 v13, 0xffff0000, v61
	v_pk_fma_f32 v[6:7], v[178:179], v[12:13], v[6:7]
	v_cvt_pk_bf16_f32 v8, v2, v3
	v_cvt_pk_bf16_f32 v9, v6, v7
	v_mov_b32_e32 v12, v5
	v_mov_b32_e32 v13, v3
	global_store_dwordx2 v[104:105], v[8:9], off offset:512 nt
	v_mov_b32_e32 v8, v4
	v_mov_b32_e32 v9, v2
	v_pk_mul_f32 v[12:13], v[12:13], v[12:13]
	v_mov_b32_e32 v107, v7
	v_pk_fma_f32 v[8:9], v[8:9], v[8:9], v[12:13]
	v_mov_b32_e32 v12, v10
	v_mov_b32_e32 v13, v6
	v_pk_mul_f32 v[106:107], v[106:107], v[106:107]
	s_nop 0
	v_pk_fma_f32 v[12:13], v[12:13], v[12:13], v[106:107]
	v_pk_add_f32 v[8:9], v[8:9], v[12:13]
	v_lshlrev_b32_e32 v12, 16, v62
	v_pk_add_f32 v[110:111], v[8:9], v[8:9] op_sel:[0,1] op_sel_hi:[1,0]
	v_lshlrev_b32_e32 v8, 16, v54
	v_and_b32_e32 v9, 0xffff0000, v54
	v_and_b32_e32 v13, 0xffff0000, v62
	s_waitcnt vmcnt(13)
	v_pk_fma_f32 v[12:13], v[180:181], v[12:13], v[8:9]
	v_lshlrev_b32_e32 v8, 16, v55
	v_and_b32_e32 v9, 0xffff0000, v55
	v_lshlrev_b32_e32 v106, 16, v63
	v_and_b32_e32 v107, 0xffff0000, v63
	v_pk_fma_f32 v[112:113], v[182:183], v[106:107], v[8:9]
	global_load_dwordx4 v[180:183], v[86:87], off
	v_cvt_pk_bf16_f32 v8, v12, v13
	v_cvt_pk_bf16_f32 v9, v112, v113
	v_mov_b32_e32 v106, v13
	v_mov_b32_e32 v107, v113
	global_store_dwordx2 v[104:105], v[8:9], off offset:1024 nt
	v_mov_b32_e32 v8, v12
	v_mov_b32_e32 v9, v112
	v_pk_mul_f32 v[106:107], v[106:107], v[106:107]
	s_nop 0
	v_pk_fma_f32 v[8:9], v[8:9], v[8:9], v[106:107]
	v_pk_add_f32 v[114:115], v[8:9], v[8:9] op_sel:[0,1] op_sel_hi:[1,0]
	v_lshlrev_b32_e32 v8, 16, v56
	v_and_b32_e32 v9, 0xffff0000, v56
	s_waitcnt vmcnt(14)
	v_pk_fma_f32 v[116:117], v[200:201], v[116:117], v[8:9]
	v_lshlrev_b32_e32 v8, 16, v57
	v_and_b32_e32 v9, 0xffff0000, v57
	v_lshlrev_b32_e32 v106, 16, v65
	v_and_b32_e32 v107, 0xffff0000, v65
	v_pk_fma_f32 v[118:119], v[202:203], v[106:107], v[8:9]
	global_load_dwordx4 v[200:203], v242, s[100:101]
	v_cvt_pk_bf16_f32 v8, v116, v117
	v_cvt_pk_bf16_f32 v9, v118, v119
	global_store_dwordx2 v[104:105], v[8:9], off offset:1536 nt
	v_mul_f32_e32 v8, v117, v117
	v_pk_fma_f32 v[122:123], v[116:117], v[116:117], v[8:9] op_sel_hi:[1,1,0]
	v_mul_f32_e32 v8, v119, v119
	v_pk_fma_f32 v[124:125], v[118:119], v[118:119], v[8:9] op_sel_hi:[1,1,0]
	v_lshlrev_b32_e32 v8, 16, v66
	v_and_b32_e32 v9, 0xffff0000, v66
	s_waitcnt vmcnt(15)
	v_pk_fma_f32 v[8:9], v[204:205], v[120:121], v[8:9]
	v_lshlrev_b32_e32 v106, 16, v67
	v_and_b32_e32 v107, 0xffff0000, v67
	v_lshlrev_b32_e32 v120, 16, v75
	v_and_b32_e32 v121, 0xffff0000, v75
	v_pk_fma_f32 v[120:121], v[206:207], v[120:121], v[106:107]
	global_load_dwordx4 v[204:207], v242, s[98:99]
	v_cvt_pk_bf16_f32 v106, v8, v9
	v_cvt_pk_bf16_f32 v107, v120, v121
	global_store_dwordx2 v[104:105], v[106:107], off offset:2048 nt
	v_pk_mul_f32 v[106:107], v[8:9], v[8:9]
	v_pk_mul_f32 v[108:109], v[120:121], v[120:121]
	v_mov_b32_e32 v111, v106
	v_mov_b32_e32 v115, v107
	v_mov_b32_e32 v123, v108
	v_mov_b32_e32 v125, v109
	v_pk_add_f32 v[106:107], v[110:111], v[114:115]
	v_pk_add_f32 v[108:109], v[122:123], v[124:125]
	v_lshlrev_b32_e32 v114, 16, v68
	v_pk_add_f32 v[106:107], v[106:107], v[108:109]
	v_and_b32_e32 v115, 0xffff0000, v68
	v_pk_add_f32 v[110:111], v[106:107], v[106:107] op_sel:[0,1] op_sel_hi:[1,0]
	v_lshlrev_b32_e32 v122, 16, v76
	v_and_b32_e32 v123, 0xffff0000, v76
	s_waitcnt vmcnt(16)
	v_pk_fma_f32 v[124:125], v[208:209], v[122:123], v[114:115]
	v_lshlrev_b32_e32 v106, 16, v69
	v_and_b32_e32 v107, 0xffff0000, v69
	v_lshlrev_b32_e32 v114, 16, v77
	v_and_b32_e32 v115, 0xffff0000, v77
	v_pk_fma_f32 v[126:127], v[210:211], v[114:115], v[106:107]
	global_load_dwordx4 v[208:211], v[88:89], off
	v_cvt_pk_bf16_f32 v106, v124, v125
	v_cvt_pk_bf16_f32 v107, v126, v127
	v_mov_b32_e32 v108, v125
	v_mov_b32_e32 v109, v127
	global_store_dwordx2 v[104:105], v[106:107], off offset:2560 nt
	v_mov_b32_e32 v106, v124
	v_mov_b32_e32 v107, v126
	v_pk_mul_f32 v[108:109], v[108:109], v[108:109]
	v_lshlrev_b32_e32 v122, 16, v70
	v_pk_fma_f32 v[106:107], v[106:107], v[106:107], v[108:109]
	v_and_b32_e32 v123, 0xffff0000, v70
	v_pk_add_f32 v[114:115], v[106:107], v[106:107] op_sel:[0,1] op_sel_hi:[1,0]
	s_waitcnt vmcnt(17)
	v_pk_fma_f32 v[128:129], v[212:213], v[128:129], v[122:123]
	v_lshlrev_b32_e32 v106, 16, v71
	v_and_b32_e32 v107, 0xffff0000, v71
	v_lshlrev_b32_e32 v122, 16, v79
	v_and_b32_e32 v123, 0xffff0000, v79
	v_pk_fma_f32 v[130:131], v[214:215], v[122:123], v[106:107]
	global_load_dwordx4 v[212:215], v243, s[100:101]
	v_cvt_pk_bf16_f32 v106, v128, v129
	v_cvt_pk_bf16_f32 v107, v130, v131
	global_store_dwordx2 v[104:105], v[106:107], off offset:3072 nt
	v_mul_f32_e32 v106, v129, v129
	v_pk_fma_f32 v[122:123], v[128:129], v[128:129], v[106:107] op_sel_hi:[1,1,0]
	v_mul_f32_e32 v106, v131, v131
	v_pk_fma_f32 v[168:169], v[130:131], v[130:131], v[106:107] op_sel_hi:[1,1,0]
	s_add_u32 s22, s15, 0x8000
	s_addc_u32 s23, s17, 0
	s_waitcnt vmcnt(18)
	v_pk_fma_f32 v[164:165], v[216:217], v[166:167], v[164:165]
	v_lshlrev_b32_e32 v106, 16, v73
	v_and_b32_e32 v107, 0xffff0000, v73
	v_lshlrev_b32_e32 v166, 16, v81
	v_and_b32_e32 v167, 0xffff0000, v81
	v_pk_fma_f32 v[166:167], v[218:219], v[166:167], v[106:107]
	global_load_dwordx4 v[216:219], v243, s[98:99]
	v_cvt_pk_bf16_f32 v106, v164, v165
	v_cvt_pk_bf16_f32 v107, v166, v167
	global_store_dwordx2 v[104:105], v[106:107], off offset:3584 nt
	v_pk_mul_f32 v[104:105], v[164:165], v[164:165]
	v_pk_mul_f32 v[106:107], v[166:167], v[166:167]
	v_mov_b32_e32 v111, v104
	v_mov_b32_e32 v115, v105
	v_mov_b32_e32 v123, v106
	v_mov_b32_e32 v169, v107
	v_pk_add_f32 v[104:105], v[110:111], v[114:115]
	v_pk_add_f32 v[106:107], v[122:123], v[168:169]
	s_nop 0
	v_pk_add_f32 v[104:105], v[104:105], v[106:107]
	s_nop 0
	v_add_f32_e32 v104, v104, v105
	s_waitcnt lgkmcnt(0)
	s_nop 1
	v_add_f32_dpp v104, v104, v104 quad_perm:[1,0,3,2] row_mask:0xf bank_mask:0xf
	s_nop 1
	v_add_f32_dpp v104, v104, v104 quad_perm:[2,3,0,1] row_mask:0xf bank_mask:0xf
	s_nop 1
	v_add_f32_dpp v104, v104, v104 row_half_mirror row_mask:0xf bank_mask:0xf
	s_nop 1
	v_add_f32_dpp v104, v104, v104 row_mirror row_mask:0xf bank_mask:0xf
	v_mov_b32_e32 v105, v104
	s_nop 1
	v_permlane16_swap_b32 v105, v104
	v_add_f32_e32 v104, v105, v104
	v_mov_b32_e32 v105, v104
	s_nop 1
	v_permlane32_swap_b32 v105, v104
	v_add_f32_e32 v104, v105, v104
	v_fmamk_f32 v104, v104, 0x3a000000, v248
	v_cmp_gt_f32_e32 vcc, s51, v104
	v_mul_f32_e32 v105, 0x4b800000, v104
	s_nop 0
	v_cndmask_b32_e32 v104, v104, v105, vcc
	v_rsq_f32_e32 v104, v104
	s_nop 0
	v_mul_f32_e32 v105, 0x45800000, v104
	v_cndmask_b32_e32 v168, v104, v105, vcc
	v_pk_mul_f32 v[10:11], v[10:11], v[168:169] op_sel_hi:[1,0]
	v_pk_mul_f32 v[4:5], v[4:5], v[168:169] op_sel_hi:[1,0]
	v_pk_mul_f32 v[2:3], v[2:3], v[168:169] op_sel_hi:[1,0]
	v_pk_mul_f32 v[116:117], v[116:117], v[168:169] op_sel_hi:[1,0]
	s_waitcnt vmcnt(19)
	v_pk_mul_f32 v[4:5], v[220:221], v[4:5]
	v_pk_mul_f32 v[10:11], v[222:223], v[10:11]
	global_load_dwordx4 v[220:223], v[90:91], off
	s_waitcnt vmcnt(18)
	v_pk_add_f32 v[104:105], v[230:231], 1.0 op_sel_hi:[1,0]
	v_pk_add_f32 v[106:107], v[228:229], 1.0 op_sel_hi:[1,0]
	global_load_dwordx4 v[228:231], v244, s[100:101]
	v_pk_fma_f32 v[104:105], v[104:105], v[10:11], v[226:227]
	v_pk_fma_f32 v[106:107], v[106:107], v[4:5], v[224:225]
	global_load_dwordx4 v[224:227], v244, s[98:99]
	v_max_f32_e64 v4, |v104|, |v105|
	v_max3_f32 v114, |v106|, |v107|, v4
	v_pk_mul_f32 v[4:5], v[6:7], v[168:169] op_sel_hi:[1,0]
	s_waitcnt vmcnt(19)
	v_pk_mul_f32 v[2:3], v[232:233], v[2:3]
	v_pk_mul_f32 v[4:5], v[234:235], v[4:5]
	global_load_dwordx4 v[232:235], v[92:93], off
	s_waitcnt vmcnt(18)
	v_pk_add_f32 v[6:7], v[254:255], 1.0 op_sel_hi:[1,0]
	v_pk_add_f32 v[10:11], v[252:253], 1.0 op_sel_hi:[1,0]
	global_load_dwordx4 v[252:255], v245, s[100:101]
	v_pk_fma_f32 v[108:109], v[6:7], v[4:5], v[238:239]
	v_pk_fma_f32 v[110:111], v[10:11], v[2:3], v[236:237]
	global_load_dwordx4 v[236:239], v245, s[98:99]
	v_max_f32_e64 v2, |v108|, |v109|
	v_max3_f32 v2, |v110|, |v111|, v2
	v_max3_f32 v122, v114, 0, v2
	v_pk_mul_f32 v[6:7], v[112:113], v[168:169] op_sel_hi:[1,0]
	v_pk_mul_f32 v[10:11], v[12:13], v[168:169] op_sel_hi:[1,0]
	s_waitcnt vmcnt(17)
	v_pk_mul_f32 v[4:5], v[182:183], v[6:7]
	v_pk_mul_f32 v[2:3], v[180:181], v[10:11]
	global_load_dwordx4 v[180:183], v[94:95], off
	s_waitcnt vmcnt(14)
	v_pk_add_f32 v[6:7], v[206:207], 1.0 op_sel_hi:[1,0]
	v_pk_add_f32 v[10:11], v[204:205], 1.0 op_sel_hi:[1,0]
	global_load_dwordx4 v[204:207], v246, s[100:101]
	v_pk_fma_f32 v[112:113], v[6:7], v[4:5], v[202:203]
	v_pk_fma_f32 v[114:115], v[10:11], v[2:3], v[200:201]
	global_load_dwordx4 v[200:203], v246, s[98:99]
	v_max_f32_e64 v2, |v112|, |v113|
	v_max3_f32 v123, |v114|, |v115|, v2
	v_pk_mul_f32 v[6:7], v[118:119], v[168:169] op_sel_hi:[1,0]
	s_waitcnt vmcnt(14)
	v_pk_mul_f32 v[2:3], v[208:209], v[116:117]
	v_pk_mul_f32 v[4:5], v[210:211], v[6:7]
	global_load_dwordx4 v[208:211], v[96:97], off
	s_waitcnt vmcnt(11)
	v_pk_add_f32 v[6:7], v[218:219], 1.0 op_sel_hi:[1,0]
	v_pk_add_f32 v[118:119], v[216:217], 1.0 op_sel_hi:[1,0]
	global_load_dwordx4 v[216:219], v247, s[100:101]
	v_pk_fma_f32 v[116:117], v[6:7], v[4:5], v[214:215]
	v_pk_fma_f32 v[118:119], v[118:119], v[2:3], v[212:213]
	global_load_dwordx4 v[212:215], v247, s[98:99]
	v_max_f32_e64 v2, |v116|, |v117|
	v_max3_f32 v2, |v118|, |v119|, v2
	v_max3_f32 v169, v122, v123, v2
	v_pk_mul_f32 v[6:7], v[120:121], v[168:169] op_sel_hi:[1,0]
	v_pk_mul_f32 v[8:9], v[8:9], v[168:169] op_sel_hi:[1,0]
	v_pk_mul_f32 v[126:127], v[126:127], v[168:169] op_sel_hi:[1,0]
	v_pk_mul_f32 v[124:125], v[124:125], v[168:169] op_sel_hi:[1,0]
	s_waitcnt vmcnt(11)
	v_pk_mul_f32 v[4:5], v[222:223], v[6:7]
	v_pk_mul_f32 v[2:3], v[220:221], v[8:9]
	s_waitcnt vmcnt(9)
	v_pk_add_f32 v[6:7], v[226:227], 1.0 op_sel_hi:[1,0]
	v_pk_add_f32 v[8:9], v[224:225], 1.0 op_sel_hi:[1,0]
	v_pk_fma_f32 v[120:121], v[6:7], v[4:5], v[230:231]
	v_pk_fma_f32 v[122:123], v[8:9], v[2:3], v[228:229]
	v_max_f32_e64 v2, |v120|, |v121|
	v_max3_f32 v170, |v122|, |v123|, v2
	s_waitcnt vmcnt(8)
	v_pk_mul_f32 v[4:5], v[126:127], v[234:235]
	v_pk_mul_f32 v[2:3], v[124:125], v[232:233]
	s_waitcnt vmcnt(6)
	v_pk_add_f32 v[12:13], v[238:239], 1.0 op_sel_hi:[1,0]
	v_pk_add_f32 v[10:11], v[236:237], 1.0 op_sel_hi:[1,0]
	v_pk_fma_f32 v[124:125], v[4:5], v[12:13], v[254:255]
	v_pk_fma_f32 v[126:127], v[2:3], v[10:11], v[252:253]
	v_max_f32_e64 v2, |v124|, |v125|
	v_max3_f32 v2, |v126|, |v127|, v2
	v_max3_f32 v169, v169, v170, v2
	v_pk_mul_f32 v[130:131], v[130:131], v[168:169] op_sel_hi:[1,0]
	v_pk_mul_f32 v[128:129], v[128:129], v[168:169] op_sel_hi:[1,0]
	v_pk_mul_f32 v[166:167], v[166:167], v[168:169] op_sel_hi:[1,0]
	v_pk_mul_f32 v[164:165], v[164:165], v[168:169] op_sel_hi:[1,0]
	s_waitcnt vmcnt(5)
	v_pk_mul_f32 v[4:5], v[130:131], v[182:183]
	v_pk_mul_f32 v[2:3], v[128:129], v[180:181]
	s_waitcnt vmcnt(3)
	v_pk_add_f32 v[12:13], v[202:203], 1.0 op_sel_hi:[1,0]
	v_pk_add_f32 v[10:11], v[200:201], 1.0 op_sel_hi:[1,0]
	v_pk_fma_f32 v[128:129], v[4:5], v[12:13], v[206:207]
	v_pk_fma_f32 v[130:131], v[2:3], v[10:11], v[204:205]
	v_max_f32_e64 v2, |v128|, |v129|
	v_max3_f32 v170, |v130|, |v131|, v2
	s_waitcnt vmcnt(2)
	v_pk_mul_f32 v[8:9], v[166:167], v[210:211]
	v_pk_mul_f32 v[6:7], v[164:165], v[208:209]
	s_waitcnt vmcnt(0)
	v_pk_add_f32 v[12:13], v[214:215], 1.0 op_sel_hi:[1,0]
	v_pk_add_f32 v[10:11], v[212:213], 1.0 op_sel_hi:[1,0]
	v_pk_fma_f32 v[4:5], v[8:9], v[12:13], v[218:219]
	v_pk_fma_f32 v[6:7], v[6:7], v[10:11], v[216:217]
	v_max_f32_e64 v2, |v4|, |v5|
	v_max3_f32 v2, |v6|, |v7|, v2
	v_max3_f32 v2, v169, v170, v2
	s_waitcnt lgkmcnt(0)
	s_nop 1
	v_max_f32_dpp v2, v2, v2 quad_perm:[1,0,3,2] row_mask:0xf bank_mask:0xf
	s_nop 1
	v_max_f32_dpp v2, v2, v2 quad_perm:[2,3,0,1] row_mask:0xf bank_mask:0xf
	s_nop 1
	v_max_f32_dpp v2, v2, v2 row_half_mirror row_mask:0xf bank_mask:0xf
	s_nop 1
	v_max_f32_dpp v2, v2, v2 row_mirror row_mask:0xf bank_mask:0xf
	v_mov_b32_e32 v3, v2
	s_nop 1
	v_permlane16_swap_b32 v3, v2
	v_max_f32_e32 v2, v3, v2
	ds_bpermute_b32 v3, v189, v2
	s_and_saveexec_b64 s[22:23], s[4:5]
	s_cbranch_execz .LBB0_3201
	s_waitcnt lgkmcnt(0)
	v_max_f32_e32 v3, v3, v3
	v_max_f32_e32 v2, v2, v2
	s_lshl_b64 s[24:25], s[18:19], 2
	v_max_f32_e32 v2, v2, v3
	s_add_u32 s24, s35, s24
	v_mul_f32_e32 v2, 0x3c010204, v2
	s_addc_u32 s25, s38, s25
	global_store_dword v17, v2, s[24:25]
